# speedup vs baseline: 1.0098x; 1.0098x over previous
_Z16closed_form_mainPKfS0_PKiPf:
	s_load_dwordx8 s[16:23], s[0:1], 0x0
	s_lshr_b32 s6, s2, 3
	v_readfirstlane_b32 s0, v0
	s_mul_hi_u32 s7, s6, 0x24924925
	s_lshr_b32 s4, s0, 6
	s_and_b32 s0, s2, 7
	s_mul_i32 s1, s7, 7
	s_bfe_u32 s5, s2, 0x10003
	s_sub_i32 s1, s6, s1
	s_mul_i32 s36, s0, 7
	s_xor_b32 s3, s4, s5
	s_add_i32 s36, s36, s1
	s_waitcnt lgkmcnt(0)
	s_mov_b64 s[28:29], s[22:23]
	v_and_b32_e32 v19, 63, v0
	s_cmp_lt_u32 s36, 52
	s_mov_b64 s[0:1], -1
	s_cbranch_scc0 .LBB0_32
	s_mul_hi_u32 s0, s6, 0x20820821
	s_lshr_b32 s38, s0, 3
	s_mul_hi_u32 s0, s7, 0x1c71c71d
	s_mul_i32 s0, s0, 9
	s_sub_i32 s0, s7, s0
	v_add_u32_e32 v2, -3, v19
	v_mad_u64_u32 v[0:1], s[0:1], s0, 57, v[2:3]
	s_mov_b64 s[24:25], s[18:19]
	v_mov_b32_e32 v1, 0x200
	v_med3_i32 v1, v0, 0, v1
	s_mul_i32 s34, s36, 10
	s_and_b32 s17, s17, 0xffff
	s_and_b32 s25, s25, 0xffff
	v_cmp_gt_u32_e64 s[0:1], 57, v2
	s_mov_b32 s19, 0x20000
	s_mov_b32 s18, 0xe0e038
	s_mov_b32 s26, 0x606018
	s_mul_i32 s35, s38, 0x70701c
	s_mul_i32 s33, s38, 0x30300c
	v_lshlrev_b32_e32 v28, 2, v1
	v_mul_u32_u24_e32 v27, 12, v1
	v_lshlrev_b32_e32 v23, 4, v19
	s_cmp_lg_u32 s4, s5
	v_sub_u32_e64 v29, s34, 2 clamp
	s_cbranch_scc0 .LBB0_15
	s_setprio 2
	s_mov_b32 s27, s19
	s_and_b32 s21, s21, 0xffff
	s_mov_b32 s22, 0x202008
	s_mov_b32 s23, s19
	s_mul_i32 s38, s38, 0x101004
	s_movk_i32 s37, 0x80
	v_add_u32_e32 v18, -1, v0
	s_movk_i32 s4, 0x201
	s_movk_i32 s5, 0x1ff
	v_cmp_gt_u32_e64 s[40:41], s4, v0
	v_cmp_gt_u32_e64 s[42:43], s5, v18
	v_mov_b32_e32 v18, 0x42c80000
	v_mov_b32_e32 v22, 0x3de38e39
	v_mov_b32_e32 v26, 0x3a3d6628
	v_mov_b32_e32 v1, 0
	s_add_i32 s4, s34, -3
	s_max_i32 s4, s4, 0
	s_mul_i32 s4, s4, 0x804
	s_add_i32 s4, s4, s38
	buffer_load_dword v29, v28, s[20:23], s4 offen nt
	s_add_i32 s4, s34, -2
	s_max_i32 s4, s4, 0
	s_mul_i32 s4, s4, 0x804
	s_add_i32 s4, s4, s38
	buffer_load_dword v2, v28, s[20:23], s4 offen nt
	s_add_i32 s5, s34, -2
	s_max_i32 s5, s5, 0
	s_mul_i32 s6, s5, 0x804
	s_add_i32 s6, s6, s35
	s_add_i32 s7, s6, 0x505014
	s_add_i32 s8, s6, 0x606018
	s_mul_i32 s9, s5, 0x180c
	s_add_i32 s9, s9, s33
	s_add_i32 s4, s34, -1
	s_max_i32 s4, s4, 0
	s_mul_i32 s4, s4, 0x804
	s_add_i32 s4, s4, s38
	buffer_load_dword v3, v28, s[20:23], s4 offen nt
	buffer_load_dwordx3 v[8:10], v27, s[24:27], s9 offen nt
	buffer_load_dword v4, v28, s[16:19], s7 offen nt
	buffer_load_dword v5, v28, s[16:19], s8 offen nt
	s_add_i32 s5, s34, -1
	s_max_i32 s5, s5, 0
	s_mul_i32 s6, s5, 0x804
	s_add_i32 s6, s6, s35
	s_add_i32 s7, s6, 0x505014
	s_add_i32 s8, s6, 0x606018
	s_mul_i32 s9, s5, 0x180c
	s_add_i32 s9, s9, s33
	s_add_i32 s4, s34, 0
	s_min_i32 s4, s4, 0x200
	s_mul_i32 s4, s4, 0x804
	s_add_i32 s4, s4, s38
	buffer_load_dword v16, v28, s[20:23], s4 offen nt
	buffer_load_dwordx3 v[12:14], v27, s[24:27], s9 offen nt
	buffer_load_dword v6, v28, s[16:19], s7 offen nt
	buffer_load_dword v7, v28, s[16:19], s8 offen nt
	s_add_i32 s5, s34, 0
	s_min_i32 s5, s5, 0x200
	s_mul_i32 s6, s5, 0x804
	s_add_i32 s6, s6, s35
	s_add_i32 s7, s6, 0x505014
	s_add_i32 s8, s6, 0x606018
	s_mul_i32 s9, s5, 0x180c
	s_add_i32 s9, s9, s33
	s_add_i32 s4, s34, 1
	s_min_i32 s4, s4, 0x200
	s_mul_i32 s4, s4, 0x804
	s_add_i32 s4, s4, s38
	buffer_load_dword v17, v28, s[20:23], s4 offen nt
	buffer_load_dwordx3 v[32:34], v27, s[24:27], s9 offen nt
	buffer_load_dword v20, v28, s[16:19], s7 offen nt
	buffer_load_dword v21, v28, s[16:19], s8 offen nt
	s_add_i32 s5, s34, 1
	s_min_i32 s5, s5, 0x200
	s_mul_i32 s6, s5, 0x804
	s_add_i32 s6, s6, s35
	s_add_i32 s7, s6, 0x505014
	s_add_i32 s8, s6, 0x606018
	s_mul_i32 s9, s5, 0x180c
	s_add_i32 s9, s9, s33
	s_add_i32 s4, s34, 2
	s_min_i32 s4, s4, 0x200
	s_mul_i32 s4, s4, 0x804
	s_add_i32 s4, s4, s38
	buffer_load_dword v30, v28, s[20:23], s4 offen nt
	buffer_load_dwordx3 v[36:38], v27, s[24:27], s9 offen nt
	buffer_load_dword v24, v28, s[16:19], s7 offen nt
	buffer_load_dword v25, v28, s[16:19], s8 offen nt
	s_waitcnt vmcnt(16)
	s_add_i32 s4, s34, -3
	s_cmpk_lt_u32 s4, 0x201
	s_cselect_b64 s[12:13], s[40:41], 0
	v_cmp_eq_u32_e64 s[14:15], s37, v29
	s_and_b64 s[14:15], s[14:15], s[12:13]
	v_cndmask_b32_e64 v31, 0, 1, s[14:15]
	s_add_i32 s4, s34, -2
	s_cmpk_lt_u32 s4, 0x201
	s_cselect_b64 s[12:13], s[40:41], 0
	v_cmp_eq_u32_e64 s[14:15], s37, v2
	s_and_b64 s[14:15], s[14:15], s[12:13]
	v_cndmask_b32_e64 v40, 0, 1, s[14:15]
	s_nop 0
	v_or_b32_dpp v41, v31, v31 wave_shr:1 row_mask:0xf bank_mask:0xf bound_ctrl:1
	v_or_b32_dpp v42, v40, v40 wave_shr:1 row_mask:0xf bank_mask:0xf bound_ctrl:1
	s_nop 1
	v_or_b32_dpp v41, v31, v41 wave_shl:1 row_mask:0xf bank_mask:0xf bound_ctrl:1
	v_or_b32_dpp v42, v40, v42 wave_shl:1 row_mask:0xf bank_mask:0xf bound_ctrl:1
	s_nop 1
	v_or_b32_dpp v43, v41, v41 wave_shr:1 row_mask:0xf bank_mask:0xf bound_ctrl:1
	v_or_b32_dpp v44, v42, v42 wave_shr:1 row_mask:0xf bank_mask:0xf bound_ctrl:1
	s_nop 1
	v_or_b32_dpp v43, v41, v43 wave_shl:1 row_mask:0xf bank_mask:0xf bound_ctrl:1
	v_or_b32_dpp v44, v42, v44 wave_shl:1 row_mask:0xf bank_mask:0xf bound_ctrl:1
	v_mov_b32_e32 v31, 0
	v_mov_b32_e32 v42, 0
	s_waitcnt vmcnt(12)
	v_mov_b32_dpp v48, v8 wave_shr:1 row_mask:0xf bank_mask:0xf bound_ctrl:1
	v_mov_b32_dpp v49, v9 wave_shr:1 row_mask:0xf bank_mask:0xf bound_ctrl:1
	v_mov_b32_dpp v50, v10 wave_shr:1 row_mask:0xf bank_mask:0xf bound_ctrl:1
	v_mov_b32_dpp v52, v8 wave_shl:1 row_mask:0xf bank_mask:0xf bound_ctrl:1
	v_mov_b32_dpp v53, v9 wave_shl:1 row_mask:0xf bank_mask:0xf bound_ctrl:1
	v_mov_b32_dpp v54, v10 wave_shl:1 row_mask:0xf bank_mask:0xf bound_ctrl:1
	s_add_i32 s4, s34, -1
	s_cmpk_lt_u32 s4, 0x201
	s_cselect_b64 s[12:13], s[40:41], 0
	v_cmp_eq_u32_e64 s[14:15], s37, v3
	s_and_b64 s[14:15], s[14:15], s[12:13]
	v_cndmask_b32_e64 v45, 0, 1, s[14:15]
	v_pk_add_f32 v[40:41], v[8:9], v[48:49]
	v_pk_mul_f32 v[46:47], v[8:9], v[8:9] op_sel_hi:[0,1]
	v_or_b32_dpp v62, v45, v45 wave_shr:1 row_mask:0xf bank_mask:0xf bound_ctrl:1
	v_pk_mul_f32 v[56:57], v[8:9], v[10:11] op_sel_hi:[1,0]
	v_or_b32_dpp v62, v45, v62 wave_shl:1 row_mask:0xf bank_mask:0xf bound_ctrl:1
	v_mul_f32_e64 v58, v9, v9
	v_mul_f32_e64 v59, v10, v10
	v_or_b32_dpp v63, v62, v62 wave_shr:1 row_mask:0xf bank_mask:0xf bound_ctrl:1
	v_add_f32_e64 v60, v10, v50
	v_pk_add_f32 v[40:41], v[40:41], v[52:53]
	v_or_b32_dpp v63, v62, v63 wave_shl:1 row_mask:0xf bank_mask:0xf bound_ctrl:1
	v_or3_b32 v45, v63, v44, v43
	v_or3_b32 v45, v45, v31, v42
	s_add_i32 s4, s34, -4
	s_cmpk_lt_u32 s4, 0x1ff
	s_cselect_b64 s[12:13], s[42:43], 0
	v_cmp_ne_u32_e64 s[30:31], 0, v45
	s_and_b64 s[30:31], s[30:31], s[12:13]
	v_cndmask_b32_e64 v45, 0, 1.0, s[30:31]
	v_pk_fma_f32 v[46:47], v[48:49], v[48:49], v[46:47] op_sel_hi:[0,1,1]
	v_pk_fma_f32 v[56:57], v[48:49], v[50:51], v[56:57] op_sel_hi:[1,0,1]
	v_fma_f32 v58, v49, v49, v58
	v_fma_f32 v59, v50, v50, v59
	v_add_f32_dpp v61, v45, v45 wave_shr:1 row_mask:0xf bank_mask:0xf bound_ctrl:1
	v_add_f32_e64 v60, v60, v54
	v_pk_fma_f32 v[46:47], v[52:53], v[52:53], v[46:47] op_sel_hi:[0,1,1]
	v_pk_fma_f32 v[56:57], v[52:53], v[54:55], v[56:57] op_sel_hi:[1,0,1]
	v_fma_f32 v58, v53, v53, v58
	v_fma_f32 v59, v54, v54, v59
	v_add_f32_dpp v61, v45, v61 wave_shl:1 row_mask:0xf bank_mask:0xf bound_ctrl:1
	v_mov_b32_dpp v66, v4 wave_shr:1 row_mask:0xf bank_mask:0xf bound_ctrl:1
	v_mov_b32_dpp v67, v5 wave_shr:1 row_mask:0xf bank_mask:0xf bound_ctrl:1
	v_mov_b32_dpp v70, v4 wave_shl:1 row_mask:0xf bank_mask:0xf bound_ctrl:1
	v_mov_b32_dpp v71, v5 wave_shl:1 row_mask:0xf bank_mask:0xf bound_ctrl:1
	v_pk_mul_f32 v[64:65], v[4:5], v[8:9] op_sel_hi:[1,0]
	v_pk_mul_f32 v[68:69], v[4:5], v[8:9] op_sel:[0,1]
	v_pk_mul_f32 v[72:73], v[4:5], v[10:11] op_sel_hi:[1,0]
	v_pk_add_f32 v[76:77], v[4:5], v[66:67]
	v_pk_fma_f32 v[64:65], v[66:67], v[48:49], v[64:65] op_sel_hi:[1,0,1]
	v_pk_fma_f32 v[68:69], v[66:67], v[48:49], v[68:69] op_sel:[0,1,0]
	v_pk_fma_f32 v[72:73], v[66:67], v[50:51], v[72:73] op_sel_hi:[1,0,1]
	v_pk_add_f32 v[76:77], v[76:77], v[70:71]
	v_pk_fma_f32 v[64:65], v[70:71], v[52:53], v[64:65] op_sel_hi:[1,0,1]
	v_pk_fma_f32 v[68:69], v[70:71], v[52:53], v[68:69] op_sel:[0,1,0]
	v_pk_fma_f32 v[72:73], v[70:71], v[54:55], v[72:73] op_sel_hi:[1,0,1]
	s_barrier
	s_add_i32 s5, s34, 2
	s_min_i32 s5, s5, 0x200
	s_mul_i32 s6, s5, 0x804
	s_add_i32 s6, s6, s35
	s_add_i32 s7, s6, 0x505014
	s_add_i32 s8, s6, 0x606018
	s_mul_i32 s9, s5, 0x180c
	s_add_i32 s9, s9, s33
	s_add_i32 s4, s34, 3
	s_min_i32 s4, s4, 0x200
	s_mul_i32 s4, s4, 0x804
	s_add_i32 s4, s4, s38
	buffer_load_dword v42, v28, s[20:23], s4 offen nt
	buffer_load_dwordx3 v[80:82], v27, s[24:27], s9 offen nt
	buffer_load_dword v66, v28, s[16:19], s7 offen nt
	buffer_load_dword v67, v28, s[16:19], s8 offen nt
	s_waitcnt vmcnt(12)
	v_mov_b32_dpp v84, v12 wave_shr:1 row_mask:0xf bank_mask:0xf bound_ctrl:1
	v_mov_b32_dpp v85, v13 wave_shr:1 row_mask:0xf bank_mask:0xf bound_ctrl:1
	v_mov_b32_dpp v86, v14 wave_shr:1 row_mask:0xf bank_mask:0xf bound_ctrl:1
	v_mov_b32_dpp v88, v12 wave_shl:1 row_mask:0xf bank_mask:0xf bound_ctrl:1
	v_mov_b32_dpp v89, v13 wave_shl:1 row_mask:0xf bank_mask:0xf bound_ctrl:1
	v_mov_b32_dpp v90, v14 wave_shl:1 row_mask:0xf bank_mask:0xf bound_ctrl:1
	s_add_i32 s4, s34, 0
	s_cmpk_lt_u32 s4, 0x201
	s_cselect_b64 s[12:13], s[40:41], 0
	v_cmp_eq_u32_e64 s[14:15], s37, v16
	s_and_b64 s[14:15], s[14:15], s[12:13]
	v_cndmask_b32_e64 v45, 0, 1, s[14:15]
	v_pk_add_f32 v[70:71], v[12:13], v[84:85]
	v_pk_mul_f32 v[74:75], v[12:13], v[12:13] op_sel_hi:[0,1]
	v_or_b32_dpp v62, v45, v45 wave_shr:1 row_mask:0xf bank_mask:0xf bound_ctrl:1
	v_pk_mul_f32 v[78:79], v[12:13], v[14:15] op_sel_hi:[1,0]
	v_or_b32_dpp v62, v45, v62 wave_shl:1 row_mask:0xf bank_mask:0xf bound_ctrl:1
	v_mul_f32_e64 v92, v13, v13
	v_mul_f32_e64 v93, v14, v14
	v_or_b32_dpp v96, v62, v62 wave_shr:1 row_mask:0xf bank_mask:0xf bound_ctrl:1
	v_add_f32_e64 v94, v14, v86
	v_pk_add_f32 v[70:71], v[70:71], v[88:89]
	v_or_b32_dpp v96, v62, v96 wave_shl:1 row_mask:0xf bank_mask:0xf bound_ctrl:1
	v_or3_b32 v45, v96, v63, v44
	v_or3_b32 v45, v45, v43, v31
	s_add_i32 s4, s34, -3
	s_cmpk_lt_u32 s4, 0x1ff
	s_cselect_b64 s[12:13], s[42:43], 0
	v_cmp_ne_u32_e64 s[30:31], 0, v45
	s_and_b64 s[30:31], s[30:31], s[12:13]
	v_cndmask_b32_e64 v45, 0, 1.0, s[30:31]
	v_pk_fma_f32 v[74:75], v[84:85], v[84:85], v[74:75] op_sel_hi:[0,1,1]
	v_pk_fma_f32 v[78:79], v[84:85], v[86:87], v[78:79] op_sel_hi:[1,0,1]
	v_fma_f32 v92, v85, v85, v92
	v_fma_f32 v93, v86, v86, v93
	v_add_f32_dpp v95, v45, v45 wave_shr:1 row_mask:0xf bank_mask:0xf bound_ctrl:1
	v_add_f32_e64 v94, v94, v90
	v_pk_fma_f32 v[74:75], v[88:89], v[88:89], v[74:75] op_sel_hi:[0,1,1]
	v_pk_fma_f32 v[78:79], v[88:89], v[90:91], v[78:79] op_sel_hi:[1,0,1]
	v_fma_f32 v92, v89, v89, v92
	v_fma_f32 v93, v90, v90, v93
	v_add_f32_dpp v95, v45, v95 wave_shl:1 row_mask:0xf bank_mask:0xf bound_ctrl:1
	v_mov_b32_dpp v100, v6 wave_shr:1 row_mask:0xf bank_mask:0xf bound_ctrl:1
	v_mov_b32_dpp v101, v7 wave_shr:1 row_mask:0xf bank_mask:0xf bound_ctrl:1
	v_mov_b32_dpp v104, v6 wave_shl:1 row_mask:0xf bank_mask:0xf bound_ctrl:1
	v_mov_b32_dpp v105, v7 wave_shl:1 row_mask:0xf bank_mask:0xf bound_ctrl:1
	v_pk_mul_f32 v[98:99], v[6:7], v[12:13] op_sel_hi:[1,0]
	v_pk_mul_f32 v[102:103], v[6:7], v[12:13] op_sel:[0,1]
	v_pk_mul_f32 v[106:107], v[6:7], v[14:15] op_sel_hi:[1,0]
	v_pk_add_f32 v[110:111], v[6:7], v[100:101]
	v_pk_fma_f32 v[98:99], v[100:101], v[84:85], v[98:99] op_sel_hi:[1,0,1]
	v_pk_fma_f32 v[102:103], v[100:101], v[84:85], v[102:103] op_sel:[0,1,0]
	v_pk_fma_f32 v[106:107], v[100:101], v[86:87], v[106:107] op_sel_hi:[1,0,1]
	v_pk_add_f32 v[110:111], v[110:111], v[104:105]
	v_pk_fma_f32 v[98:99], v[104:105], v[88:89], v[98:99] op_sel_hi:[1,0,1]
	v_pk_fma_f32 v[102:103], v[104:105], v[88:89], v[102:103] op_sel:[0,1,0]
	v_pk_fma_f32 v[106:107], v[104:105], v[90:91], v[106:107] op_sel_hi:[1,0,1]
	s_barrier
	s_add_i32 s5, s34, 3
	s_min_i32 s5, s5, 0x200
	s_mul_i32 s6, s5, 0x804
	s_add_i32 s6, s6, s35
	s_add_i32 s7, s6, 0x505014
	s_add_i32 s8, s6, 0x606018
	s_mul_i32 s9, s5, 0x180c
	s_add_i32 s9, s9, s33
	s_add_i32 s4, s34, 4
	s_min_i32 s4, s4, 0x200
	s_mul_i32 s4, s4, 0x804
	s_add_i32 s4, s4, s38
	buffer_load_dword v29, v28, s[20:23], s4 offen nt
	buffer_load_dwordx3 v[112:114], v27, s[24:27], s9 offen nt
	buffer_load_dword v100, v28, s[16:19], s7 offen nt
	buffer_load_dword v101, v28, s[16:19], s8 offen nt
	s_waitcnt vmcnt(12)
	v_mov_b32_dpp v116, v32 wave_shr:1 row_mask:0xf bank_mask:0xf bound_ctrl:1
	v_mov_b32_dpp v117, v33 wave_shr:1 row_mask:0xf bank_mask:0xf bound_ctrl:1
	v_mov_b32_dpp v118, v34 wave_shr:1 row_mask:0xf bank_mask:0xf bound_ctrl:1
	v_mov_b32_dpp v120, v32 wave_shl:1 row_mask:0xf bank_mask:0xf bound_ctrl:1
	v_mov_b32_dpp v121, v33 wave_shl:1 row_mask:0xf bank_mask:0xf bound_ctrl:1
	v_mov_b32_dpp v122, v34 wave_shl:1 row_mask:0xf bank_mask:0xf bound_ctrl:1
	s_add_i32 s4, s34, 1
	s_cmpk_lt_u32 s4, 0x201
	s_cselect_b64 s[12:13], s[40:41], 0
	v_cmp_eq_u32_e64 s[14:15], s37, v17
	s_and_b64 s[14:15], s[14:15], s[12:13]
	v_cndmask_b32_e64 v31, 0, 1, s[14:15]
	v_pk_add_f32 v[104:105], v[32:33], v[116:117]
	v_pk_mul_f32 v[108:109], v[32:33], v[32:33] op_sel_hi:[0,1]
	v_or_b32_dpp v45, v31, v31 wave_shr:1 row_mask:0xf bank_mask:0xf bound_ctrl:1
	v_pk_mul_f32 v[124:125], v[32:33], v[34:35] op_sel_hi:[1,0]
	v_or_b32_dpp v45, v31, v45 wave_shl:1 row_mask:0xf bank_mask:0xf bound_ctrl:1
	v_mul_f32_e64 v126, v33, v33
	v_mul_f32_e64 v127, v34, v34
	v_or_b32_dpp v62, v45, v45 wave_shr:1 row_mask:0xf bank_mask:0xf bound_ctrl:1
	v_add_f32_e64 v128, v34, v118
	v_pk_add_f32 v[104:105], v[104:105], v[120:121]
	v_or_b32_dpp v62, v45, v62 wave_shl:1 row_mask:0xf bank_mask:0xf bound_ctrl:1
	v_or3_b32 v31, v62, v96, v63
	v_or3_b32 v31, v31, v44, v43
	s_add_i32 s4, s34, -2
	s_cmpk_lt_u32 s4, 0x1ff
	s_cselect_b64 s[12:13], s[42:43], 0
	v_cmp_ne_u32_e64 s[30:31], 0, v31
	s_and_b64 s[30:31], s[30:31], s[12:13]
	v_cndmask_b32_e64 v31, 0, 1.0, s[30:31]
	v_pk_fma_f32 v[108:109], v[116:117], v[116:117], v[108:109] op_sel_hi:[0,1,1]
	v_pk_fma_f32 v[124:125], v[116:117], v[118:119], v[124:125] op_sel_hi:[1,0,1]
	v_fma_f32 v126, v117, v117, v126
	v_fma_f32 v127, v118, v118, v127
	v_add_f32_dpp v129, v31, v31 wave_shr:1 row_mask:0xf bank_mask:0xf bound_ctrl:1
	v_add_f32_e64 v128, v128, v122
	v_pk_fma_f32 v[108:109], v[120:121], v[120:121], v[108:109] op_sel_hi:[0,1,1]
	v_pk_fma_f32 v[124:125], v[120:121], v[122:123], v[124:125] op_sel_hi:[1,0,1]
	v_fma_f32 v126, v121, v121, v126
	v_fma_f32 v127, v122, v122, v127
	v_add_f32_dpp v129, v31, v129 wave_shl:1 row_mask:0xf bank_mask:0xf bound_ctrl:1
	v_pk_add_f32 v[130:131], v[70:71], v[104:105]
	v_pk_add_f32 v[132:133], v[40:41], v[130:131]
	v_pk_add_f32 v[40:41], v[74:75], v[108:109]
	v_pk_add_f32 v[70:71], v[46:47], v[40:41]
	v_pk_add_f32 v[46:47], v[78:79], v[124:125]
	v_pk_add_f32 v[74:75], v[56:57], v[46:47]
	v_pk_add_f32 v[56:57], v[92:93], v[126:127]
	v_pk_add_f32 v[78:79], v[58:59], v[56:57]
	v_pk_add_f32 v[58:59], v[94:95], v[128:129]
	v_pk_add_f32 v[92:93], v[60:61], v[58:59]
	v_mul_f32_e64 v136, v132, v22
	v_mul_f32_e64 v137, v133, v22
	v_mul_f32_e64 v138, v92, v22
	v_fma_f32 v31, v70, v22, v26
	v_mul_f32_e64 v45, v71, v22
	v_mul_f32_e64 v97, v74, v22
	v_fma_f32 v60, v78, v22, v26
	v_mul_f32_e64 v61, v75, v22
	v_fma_f32 v94, v79, v22, v26
	v_fma_f32 v31, -v136, v136, v31
	v_fma_f32 v45, -v136, v137, v45
	v_fma_f32 v97, -v136, v138, v97
	v_fma_f32 v60, -v137, v137, v60
	v_fma_f32 v61, -v137, v138, v61
	v_fma_f32 v94, -v138, v138, v94
	v_mul_f32_e64 v95, v61, v61
	v_mul_f32_e64 v134, v45, v94
	v_mul_f32_e64 v135, v97, v60
	v_mul_f32_e64 v148, v97, v97
	v_mul_f32_e64 v149, v31, v61
	v_mul_f32_e64 v150, v45, v45
	v_fma_f32 v95, v60, v94, -v95
	v_fma_f32 v134, v97, v61, -v134
	v_fma_f32 v135, v45, v61, -v135
	v_fma_f32 v148, v31, v94, -v148
	v_fma_f32 v149, v45, v97, -v149
	v_fma_f32 v150, v31, v60, -v150
	v_mul_f32_e64 v151, v31, v95
	v_fma_f32 v151, v45, v134, v151
	v_fma_f32 v151, v97, v135, v151
	v_rcp_f32_e32 v151, v151
	v_cmp_ne_u32_e64 vcc, s37, v2
	v_mul_f32_e64 v151, v151, v22
	v_cndmask_b32_e64 v151, 0, v151, s[30:31]
	v_cndmask_b32_e64 v31, 0, v18, vcc
	v_cndmask_b32_e64 v145, 0, v22, s[30:31]
	v_mul_f32_e64 v139, v95, v151
	v_mul_f32_e64 v140, v134, v151
	v_mul_f32_e64 v141, v135, v151
	v_mul_f32_e64 v142, v148, v151
	v_mul_f32_e64 v143, v149, v151
	v_mul_f32_e64 v144, v150, v151
	v_add_f32_e64 v146, v93, v31
	v_mov_b32_e32 v147, v2
	ds_write_b128 v23, v[136:139]
	ds_write_b128 v23, v[140:143] offset:1024
	ds_write_b128 v23, v[144:147] offset:2048
	v_mov_b32_dpp v70, v20 wave_shr:1 row_mask:0xf bank_mask:0xf bound_ctrl:1
	v_mov_b32_dpp v71, v21 wave_shr:1 row_mask:0xf bank_mask:0xf bound_ctrl:1
	v_mov_b32_dpp v74, v20 wave_shl:1 row_mask:0xf bank_mask:0xf bound_ctrl:1
	v_mov_b32_dpp v75, v21 wave_shl:1 row_mask:0xf bank_mask:0xf bound_ctrl:1
	v_pk_mul_f32 v[60:61], v[20:21], v[32:33] op_sel_hi:[1,0]
	v_pk_mul_f32 v[92:93], v[20:21], v[32:33] op_sel:[0,1]
	v_pk_mul_f32 v[132:133], v[20:21], v[34:35] op_sel_hi:[1,0]
	v_pk_add_f32 v[148:149], v[20:21], v[70:71]
	v_pk_fma_f32 v[60:61], v[70:71], v[116:117], v[60:61] op_sel_hi:[1,0,1]
	v_pk_fma_f32 v[92:93], v[70:71], v[116:117], v[92:93] op_sel:[0,1,0]
	v_pk_fma_f32 v[132:133], v[70:71], v[118:119], v[132:133] op_sel_hi:[1,0,1]
	v_pk_add_f32 v[148:149], v[148:149], v[74:75]
	v_pk_fma_f32 v[60:61], v[74:75], v[120:121], v[60:61] op_sel_hi:[1,0,1]
	v_pk_fma_f32 v[92:93], v[74:75], v[120:121], v[92:93] op_sel:[0,1,0]
	v_pk_fma_f32 v[132:133], v[74:75], v[122:123], v[132:133] op_sel_hi:[1,0,1]
	s_waitcnt lgkmcnt(0)
	s_barrier
	s_add_i32 s5, s34, 4
	s_min_i32 s5, s5, 0x200
	s_mul_i32 s6, s5, 0x804
	s_add_i32 s6, s6, s35
	s_add_i32 s7, s6, 0x505014
	s_add_i32 s8, s6, 0x606018
	s_mul_i32 s9, s5, 0x180c
	s_add_i32 s9, s9, s33
	s_add_i32 s4, s34, 5
	s_min_i32 s4, s4, 0x200
	s_mul_i32 s4, s4, 0x804
	s_add_i32 s4, s4, s38
	buffer_load_dword v2, v28, s[20:23], s4 offen nt
	buffer_load_dwordx3 v[152:154], v27, s[24:27], s9 offen nt
	buffer_load_dword v70, v28, s[16:19], s7 offen nt
	buffer_load_dword v71, v28, s[16:19], s8 offen nt
	v_pk_add_f32 v[74:75], v[110:111], v[148:149]
	v_pk_add_f32 v[78:79], v[76:77], v[74:75]
	v_pk_add_f32 v[94:95], v[98:99], v[60:61]
	v_pk_add_f32 v[76:77], v[64:65], v[94:95]
	v_pk_add_f32 v[98:99], v[102:103], v[92:93]
	v_pk_add_f32 v[64:65], v[68:69], v[98:99]
	v_pk_add_f32 v[102:103], v[106:107], v[132:133]
	v_pk_add_f32 v[68:69], v[72:73], v[102:103]
	v_pk_fma_f32 v[76:77], v[136:137], v[78:79], v[76:77] op_sel_hi:[0,1,1] neg_lo:[1,0,0] neg_hi:[1,0,0]
	v_pk_fma_f32 v[64:65], v[136:137], v[78:79], v[64:65] op_sel:[1,0,0] neg_lo:[1,0,0] neg_hi:[1,0,0]
	v_pk_fma_f32 v[68:69], v[138:139], v[78:79], v[68:69] op_sel_hi:[0,1,1] neg_lo:[1,0,0] neg_hi:[1,0,0]
	v_pk_mul_f32 v[106:107], v[138:139], v[76:77] op_sel:[1,0]
	v_pk_mul_f32 v[110:111], v[140:141], v[76:77] op_sel_hi:[0,1]
	v_pk_mul_f32 v[134:135], v[140:141], v[76:77] op_sel:[1,0]
	v_pk_fma_f32 v[106:107], v[140:141], v[64:65], v[106:107] op_sel_hi:[0,1,1]
	v_pk_fma_f32 v[110:111], v[142:143], v[64:65], v[110:111] op_sel_hi:[0,1,1]
	v_pk_fma_f32 v[134:135], v[142:143], v[64:65], v[134:135] op_sel:[1,0,0]
	v_pk_fma_f32 v[106:107], v[140:141], v[68:69], v[106:107] op_sel:[1,0,0]
	v_pk_fma_f32 v[110:111], v[142:143], v[68:69], v[110:111] op_sel:[1,0,0]
	v_pk_fma_f32 v[134:135], v[144:145], v[68:69], v[134:135] op_sel_hi:[0,1,1]
	v_pk_mul_f32 v[72:73], v[136:137], v[106:107] op_sel_hi:[0,1]
	v_pk_fma_f32 v[72:73], v[136:137], v[110:111], v[72:73] op_sel:[1,0,0]
	v_pk_fma_f32 v[72:73], v[138:139], v[134:135], v[72:73] op_sel_hi:[0,1,1]
	v_pk_fma_f32 v[72:73], v[144:145], v[78:79], v[72:73] op_sel:[1,0,0] neg_lo:[0,0,1] neg_hi:[0,0,1]
	s_waitcnt vmcnt(12)
	v_mov_b32_dpp v8, v36 wave_shr:1 row_mask:0xf bank_mask:0xf bound_ctrl:1
	v_mov_b32_dpp v9, v37 wave_shr:1 row_mask:0xf bank_mask:0xf bound_ctrl:1
	v_mov_b32_dpp v10, v38 wave_shr:1 row_mask:0xf bank_mask:0xf bound_ctrl:1
	v_mov_b32_dpp v48, v36 wave_shl:1 row_mask:0xf bank_mask:0xf bound_ctrl:1
	v_mov_b32_dpp v49, v37 wave_shl:1 row_mask:0xf bank_mask:0xf bound_ctrl:1
	v_mov_b32_dpp v50, v38 wave_shl:1 row_mask:0xf bank_mask:0xf bound_ctrl:1
	s_add_i32 s4, s34, 2
	s_cmpk_lt_u32 s4, 0x201
	s_cselect_b64 s[12:13], s[40:41], 0
	v_cmp_eq_u32_e64 s[14:15], s37, v30
	s_and_b64 s[14:15], s[14:15], s[12:13]
	v_cndmask_b32_e64 v31, 0, 1, s[14:15]
	v_pk_add_f32 v[4:5], v[36:37], v[8:9]
	v_pk_mul_f32 v[52:53], v[36:37], v[36:37] op_sel_hi:[0,1]
	v_or_b32_dpp v43, v31, v31 wave_shr:1 row_mask:0xf bank_mask:0xf bound_ctrl:1
	v_pk_mul_f32 v[54:55], v[36:37], v[38:39] op_sel_hi:[1,0]
	v_or_b32_dpp v43, v31, v43 wave_shl:1 row_mask:0xf bank_mask:0xf bound_ctrl:1
	v_mul_f32_e64 v64, v37, v37
	v_mul_f32_e64 v65, v38, v38
	v_or_b32_dpp v45, v43, v43 wave_shr:1 row_mask:0xf bank_mask:0xf bound_ctrl:1
	v_add_f32_e64 v68, v38, v10
	v_pk_add_f32 v[4:5], v[4:5], v[48:49]
	v_or_b32_dpp v45, v43, v45 wave_shl:1 row_mask:0xf bank_mask:0xf bound_ctrl:1
	v_or3_b32 v31, v45, v62, v96
	v_or3_b32 v31, v31, v63, v44
	s_add_i32 s4, s34, -1
	s_cmpk_lt_u32 s4, 0x1ff
	s_cselect_b64 s[12:13], s[42:43], 0
	v_cmp_ne_u32_e64 s[30:31], 0, v31
	s_and_b64 s[30:31], s[30:31], s[12:13]
	v_cndmask_b32_e64 v31, 0, 1.0, s[30:31]
	v_pk_fma_f32 v[52:53], v[8:9], v[8:9], v[52:53] op_sel_hi:[0,1,1]
	v_pk_fma_f32 v[54:55], v[8:9], v[10:11], v[54:55] op_sel_hi:[1,0,1]
	v_fma_f32 v64, v9, v9, v64
	v_fma_f32 v65, v10, v10, v65
	v_add_f32_dpp v69, v31, v31 wave_shr:1 row_mask:0xf bank_mask:0xf bound_ctrl:1
	v_add_f32_e64 v68, v68, v50
	v_pk_fma_f32 v[52:53], v[48:49], v[48:49], v[52:53] op_sel_hi:[0,1,1]
	v_pk_fma_f32 v[54:55], v[48:49], v[50:51], v[54:55] op_sel_hi:[1,0,1]
	v_fma_f32 v64, v49, v49, v64
	v_fma_f32 v65, v50, v50, v65
	v_add_f32_dpp v69, v31, v69 wave_shl:1 row_mask:0xf bank_mask:0xf bound_ctrl:1
	v_pk_add_f32 v[76:77], v[130:131], v[4:5]
	v_pk_add_f32 v[78:79], v[40:41], v[52:53]
	v_pk_add_f32 v[40:41], v[46:47], v[54:55]
	v_pk_add_f32 v[46:47], v[56:57], v[64:65]
	v_pk_add_f32 v[56:57], v[58:59], v[68:69]
	v_mul_f32_e64 v136, v76, v22
	v_mul_f32_e64 v137, v77, v22
	v_mul_f32_e64 v138, v56, v22
	v_fma_f32 v31, v78, v22, v26
	v_mul_f32_e64 v43, v79, v22
	v_mul_f32_e64 v97, v40, v22
	v_fma_f32 v58, v46, v22, v26
	v_mul_f32_e64 v59, v41, v22
	v_fma_f32 v130, v47, v22, v26
	v_fma_f32 v31, -v136, v136, v31
	v_fma_f32 v43, -v136, v137, v43
	v_fma_f32 v97, -v136, v138, v97
	v_fma_f32 v58, -v137, v137, v58
	v_fma_f32 v59, -v137, v138, v59
	v_fma_f32 v130, -v138, v138, v130
	v_mul_f32_e64 v131, v59, v59
	v_mul_f32_e64 v150, v43, v130
	v_mul_f32_e64 v151, v97, v58
	v_mul_f32_e64 v156, v97, v97
	v_mul_f32_e64 v157, v31, v59
	v_mul_f32_e64 v158, v43, v43
	v_fma_f32 v131, v58, v130, -v131
	v_fma_f32 v150, v97, v59, -v150
	v_fma_f32 v151, v43, v59, -v151
	v_fma_f32 v156, v31, v130, -v156
	v_fma_f32 v157, v43, v97, -v157
	v_fma_f32 v158, v31, v58, -v158
	v_mul_f32_e64 v159, v31, v131
	v_fma_f32 v159, v43, v150, v159
	v_fma_f32 v159, v97, v151, v159
	v_rcp_f32_e32 v159, v159
	v_cmp_ne_u32_e64 vcc, s37, v3
	v_mul_f32_e64 v159, v159, v22
	v_cndmask_b32_e64 v159, 0, v159, s[30:31]
	v_cndmask_b32_e64 v31, 0, v18, vcc
	v_cndmask_b32_e64 v145, 0, v22, s[30:31]
	v_mul_f32_e64 v139, v131, v159
	v_mul_f32_e64 v140, v150, v159
	v_mul_f32_e64 v141, v151, v159
	v_mul_f32_e64 v142, v156, v159
	v_mul_f32_e64 v143, v157, v159
	v_mul_f32_e64 v144, v158, v159
	v_add_f32_e64 v146, v57, v31
	v_mov_b32_e32 v147, v3
	ds_write_b128 v23, v[136:139] offset:3072
	ds_write_b128 v23, v[140:143] offset:4096
	ds_write_b128 v23, v[144:147] offset:5120
	v_mov_b32_dpp v46, v24 wave_shr:1 row_mask:0xf bank_mask:0xf bound_ctrl:1
	v_mov_b32_dpp v47, v25 wave_shr:1 row_mask:0xf bank_mask:0xf bound_ctrl:1
	v_mov_b32_dpp v58, v24 wave_shl:1 row_mask:0xf bank_mask:0xf bound_ctrl:1
	v_mov_b32_dpp v59, v25 wave_shl:1 row_mask:0xf bank_mask:0xf bound_ctrl:1
	v_pk_mul_f32 v[40:41], v[24:25], v[36:37] op_sel_hi:[1,0]
	v_pk_mul_f32 v[56:57], v[24:25], v[36:37] op_sel:[0,1]
	v_pk_mul_f32 v[76:77], v[24:25], v[38:39] op_sel_hi:[1,0]
	v_pk_add_f32 v[156:157], v[24:25], v[46:47]
	v_pk_fma_f32 v[40:41], v[46:47], v[8:9], v[40:41] op_sel_hi:[1,0,1]
	v_pk_fma_f32 v[56:57], v[46:47], v[8:9], v[56:57] op_sel:[0,1,0]
	v_pk_fma_f32 v[76:77], v[46:47], v[10:11], v[76:77] op_sel_hi:[1,0,1]
	v_pk_add_f32 v[156:157], v[156:157], v[58:59]
	v_pk_fma_f32 v[40:41], v[58:59], v[48:49], v[40:41] op_sel_hi:[1,0,1]
	v_pk_fma_f32 v[56:57], v[58:59], v[48:49], v[56:57] op_sel:[0,1,0]
	v_pk_fma_f32 v[76:77], v[58:59], v[50:51], v[76:77] op_sel_hi:[1,0,1]
	s_waitcnt lgkmcnt(0)
	s_barrier
	s_add_i32 s5, s34, 5
	s_min_i32 s5, s5, 0x200
	s_mul_i32 s6, s5, 0x804
	s_add_i32 s6, s6, s35
	s_add_i32 s7, s6, 0x505014
	s_add_i32 s8, s6, 0x606018
	s_mul_i32 s9, s5, 0x180c
	s_add_i32 s9, s9, s33
	s_add_i32 s4, s34, 6
	s_min_i32 s4, s4, 0x200
	s_mul_i32 s4, s4, 0x804
	s_add_i32 s4, s4, s38
	buffer_load_dword v3, v28, s[20:23], s4 offen nt
	buffer_load_dwordx3 v[160:162], v27, s[24:27], s9 offen nt
	buffer_load_dword v46, v28, s[16:19], s7 offen nt
	buffer_load_dword v47, v28, s[16:19], s8 offen nt
	v_pk_add_f32 v[58:59], v[74:75], v[156:157]
	v_pk_add_f32 v[164:165], v[94:95], v[40:41]
	v_pk_add_f32 v[168:169], v[98:99], v[56:57]
	v_pk_add_f32 v[172:173], v[102:103], v[76:77]
	v_pk_fma_f32 v[164:165], v[136:137], v[58:59], v[164:165] op_sel_hi:[0,1,1] neg_lo:[1,0,0] neg_hi:[1,0,0]
	v_pk_fma_f32 v[168:169], v[136:137], v[58:59], v[168:169] op_sel:[1,0,0] neg_lo:[1,0,0] neg_hi:[1,0,0]
	v_pk_fma_f32 v[172:173], v[138:139], v[58:59], v[172:173] op_sel_hi:[0,1,1] neg_lo:[1,0,0] neg_hi:[1,0,0]
	v_pk_mul_f32 v[74:75], v[138:139], v[164:165] op_sel:[1,0]
	v_pk_mul_f32 v[78:79], v[140:141], v[164:165] op_sel_hi:[0,1]
	v_pk_mul_f32 v[94:95], v[140:141], v[164:165] op_sel:[1,0]
	v_pk_fma_f32 v[74:75], v[140:141], v[168:169], v[74:75] op_sel_hi:[0,1,1]
	v_pk_fma_f32 v[78:79], v[142:143], v[168:169], v[78:79] op_sel_hi:[0,1,1]
	v_pk_fma_f32 v[94:95], v[142:143], v[168:169], v[94:95] op_sel:[1,0,0]
	v_pk_fma_f32 v[74:75], v[140:141], v[172:173], v[74:75] op_sel:[1,0,0]
	v_pk_fma_f32 v[78:79], v[142:143], v[172:173], v[78:79] op_sel:[1,0,0]
	v_pk_fma_f32 v[94:95], v[144:145], v[172:173], v[94:95] op_sel_hi:[0,1,1]
	v_pk_mul_f32 v[176:177], v[136:137], v[74:75] op_sel_hi:[0,1]
	v_pk_fma_f32 v[176:177], v[136:137], v[78:79], v[176:177] op_sel:[1,0,0]
	v_pk_fma_f32 v[176:177], v[138:139], v[94:95], v[176:177] op_sel_hi:[0,1,1]
	v_pk_fma_f32 v[176:177], v[144:145], v[58:59], v[176:177] op_sel:[1,0,0] neg_lo:[0,0,1] neg_hi:[0,0,1]
	s_waitcnt vmcnt(12)
	v_mov_b32_dpp v12, v80 wave_shr:1 row_mask:0xf bank_mask:0xf bound_ctrl:1
	v_mov_b32_dpp v13, v81 wave_shr:1 row_mask:0xf bank_mask:0xf bound_ctrl:1
	v_mov_b32_dpp v14, v82 wave_shr:1 row_mask:0xf bank_mask:0xf bound_ctrl:1
	v_mov_b32_dpp v84, v80 wave_shl:1 row_mask:0xf bank_mask:0xf bound_ctrl:1
	v_mov_b32_dpp v85, v81 wave_shl:1 row_mask:0xf bank_mask:0xf bound_ctrl:1
	v_mov_b32_dpp v86, v82 wave_shl:1 row_mask:0xf bank_mask:0xf bound_ctrl:1
	s_add_i32 s4, s34, 3
	s_cmpk_lt_u32 s4, 0x201
	s_cselect_b64 s[12:13], s[40:41], 0
	v_cmp_eq_u32_e64 s[14:15], s37, v42
	s_and_b64 s[14:15], s[14:15], s[12:13]
	v_cndmask_b32_e64 v31, 0, 1, s[14:15]
	v_pk_add_f32 v[6:7], v[80:81], v[12:13]
	v_pk_mul_f32 v[58:59], v[80:81], v[80:81] op_sel_hi:[0,1]
	v_or_b32_dpp v43, v31, v31 wave_shr:1 row_mask:0xf bank_mask:0xf bound_ctrl:1
	v_pk_mul_f32 v[88:89], v[80:81], v[82:83] op_sel_hi:[1,0]
	v_or_b32_dpp v43, v31, v43 wave_shl:1 row_mask:0xf bank_mask:0xf bound_ctrl:1
	v_mul_f32_e64 v90, v81, v81
	v_mul_f32_e64 v91, v82, v82
	v_or_b32_dpp v44, v43, v43 wave_shr:1 row_mask:0xf bank_mask:0xf bound_ctrl:1
	v_add_f32_e64 v98, v82, v14
	v_pk_add_f32 v[6:7], v[6:7], v[84:85]
	v_or_b32_dpp v44, v43, v44 wave_shl:1 row_mask:0xf bank_mask:0xf bound_ctrl:1
	v_or3_b32 v31, v44, v45, v62
	v_or3_b32 v31, v31, v96, v63
	s_add_i32 s4, s34, 0
	s_cmpk_lt_u32 s4, 0x1ff
	s_cselect_b64 s[12:13], s[42:43], 0
	v_cmp_ne_u32_e64 s[30:31], 0, v31
	s_and_b64 s[30:31], s[30:31], s[12:13]
	v_cndmask_b32_e64 v31, 0, 1.0, s[30:31]
	v_pk_fma_f32 v[58:59], v[12:13], v[12:13], v[58:59] op_sel_hi:[0,1,1]
	v_pk_fma_f32 v[88:89], v[12:13], v[14:15], v[88:89] op_sel_hi:[1,0,1]
	v_fma_f32 v90, v13, v13, v90
	v_fma_f32 v91, v14, v14, v91
	v_add_f32_dpp v99, v31, v31 wave_shr:1 row_mask:0xf bank_mask:0xf bound_ctrl:1
	v_add_f32_e64 v98, v98, v86
	v_pk_fma_f32 v[58:59], v[84:85], v[84:85], v[58:59] op_sel_hi:[0,1,1]
	v_pk_fma_f32 v[88:89], v[84:85], v[86:87], v[88:89] op_sel_hi:[1,0,1]
	v_fma_f32 v90, v85, v85, v90
	v_fma_f32 v91, v86, v86, v91
	v_add_f32_dpp v99, v31, v99 wave_shl:1 row_mask:0xf bank_mask:0xf bound_ctrl:1
	v_pk_add_f32 v[102:103], v[4:5], v[6:7]
	v_pk_add_f32 v[130:131], v[104:105], v[102:103]
	v_pk_add_f32 v[138:139], v[52:53], v[58:59]
	v_pk_add_f32 v[4:5], v[108:109], v[138:139]
	v_pk_add_f32 v[142:143], v[54:55], v[88:89]
	v_pk_add_f32 v[52:53], v[124:125], v[142:143]
	v_pk_add_f32 v[104:105], v[64:65], v[90:91]
	v_pk_add_f32 v[54:55], v[126:127], v[104:105]
	v_pk_add_f32 v[126:127], v[68:69], v[98:99]
	v_pk_add_f32 v[64:65], v[128:129], v[126:127]
	v_mul_f32_e64 v144, v130, v22
	v_mul_f32_e64 v145, v131, v22
	v_mul_f32_e64 v146, v64, v22
	v_fma_f32 v31, v4, v22, v26
	v_mul_f32_e64 v43, v5, v22
	v_mul_f32_e64 v97, v52, v22
	v_fma_f32 v68, v54, v22, v26
	v_mul_f32_e64 v69, v53, v22
	v_fma_f32 v108, v55, v22, v26
	v_fma_f32 v31, -v144, v144, v31
	v_fma_f32 v43, -v144, v145, v43
	v_fma_f32 v97, -v144, v146, v97
	v_fma_f32 v68, -v145, v145, v68
	v_fma_f32 v69, -v145, v146, v69
	v_fma_f32 v108, -v146, v146, v108
	v_mul_f32_e64 v109, v69, v69
	v_mul_f32_e64 v124, v43, v108
	v_mul_f32_e64 v125, v97, v68
	v_mul_f32_e64 v128, v97, v97
	v_mul_f32_e64 v129, v31, v69
	v_mul_f32_e64 v136, v43, v43
	v_fma_f32 v109, v68, v108, -v109
	v_fma_f32 v124, v97, v69, -v124
	v_fma_f32 v125, v43, v69, -v125
	v_fma_f32 v128, v31, v108, -v128
	v_fma_f32 v129, v43, v97, -v129
	v_fma_f32 v136, v31, v68, -v136
	v_mul_f32_e64 v137, v31, v109
	v_fma_f32 v137, v43, v124, v137
	v_fma_f32 v137, v97, v125, v137
	v_rcp_f32_e32 v137, v137
	v_cmp_ne_u32_e64 vcc, s37, v16
	v_mul_f32_e64 v137, v137, v22
	v_cndmask_b32_e64 v137, 0, v137, s[30:31]
	v_cndmask_b32_e64 v31, 0, v18, vcc
	v_cndmask_b32_e64 v169, 0, v22, s[30:31]
	v_mul_f32_e64 v147, v109, v137
	v_mul_f32_e64 v164, v124, v137
	v_mul_f32_e64 v165, v125, v137
	v_mul_f32_e64 v166, v128, v137
	v_mul_f32_e64 v167, v129, v137
	v_mul_f32_e64 v168, v136, v137
	v_add_f32_e64 v170, v65, v31
	v_mov_b32_e32 v171, v16
	ds_write_b128 v23, v[144:147]
	ds_write_b128 v23, v[164:167] offset:1024
	ds_write_b128 v23, v[168:171] offset:2048
	v_mov_b32_dpp v4, v66 wave_shr:1 row_mask:0xf bank_mask:0xf bound_ctrl:1
	v_mov_b32_dpp v5, v67 wave_shr:1 row_mask:0xf bank_mask:0xf bound_ctrl:1
	v_mov_b32_dpp v52, v66 wave_shl:1 row_mask:0xf bank_mask:0xf bound_ctrl:1
	v_mov_b32_dpp v53, v67 wave_shl:1 row_mask:0xf bank_mask:0xf bound_ctrl:1
	v_pk_mul_f32 v[54:55], v[66:67], v[80:81] op_sel_hi:[1,0]
	v_pk_mul_f32 v[130:131], v[66:67], v[80:81] op_sel:[0,1]
	v_pk_mul_f32 v[150:151], v[66:67], v[82:83] op_sel_hi:[1,0]
	v_pk_add_f32 v[158:159], v[66:67], v[4:5]
	v_pk_fma_f32 v[54:55], v[4:5], v[12:13], v[54:55] op_sel_hi:[1,0,1]
	v_pk_fma_f32 v[130:131], v[4:5], v[12:13], v[130:131] op_sel:[0,1,0]
	v_pk_fma_f32 v[150:151], v[4:5], v[14:15], v[150:151] op_sel_hi:[1,0,1]
	v_pk_add_f32 v[158:159], v[158:159], v[52:53]
	v_pk_fma_f32 v[54:55], v[52:53], v[84:85], v[54:55] op_sel_hi:[1,0,1]
	v_pk_fma_f32 v[130:131], v[52:53], v[84:85], v[130:131] op_sel:[0,1,0]
	v_pk_fma_f32 v[150:151], v[52:53], v[86:87], v[150:151] op_sel_hi:[1,0,1]
	s_waitcnt lgkmcnt(0)
	s_barrier
	s_add_i32 s5, s34, 6
	s_min_i32 s5, s5, 0x200
	s_mul_i32 s6, s5, 0x804
	s_add_i32 s6, s6, s35
	s_add_i32 s7, s6, 0x505014
	s_add_i32 s8, s6, 0x606018
	s_mul_i32 s9, s5, 0x180c
	s_add_i32 s9, s9, s33
	s_add_i32 s4, s34, 7
	s_min_i32 s4, s4, 0x200
	s_mul_i32 s4, s4, 0x804
	s_add_i32 s4, s4, s38
	buffer_load_dword v16, v28, s[20:23], s4 offen nt
	buffer_load_dwordx3 v[172:174], v27, s[24:27], s9 offen nt
	buffer_load_dword v4, v28, s[16:19], s7 offen nt
	buffer_load_dword v5, v28, s[16:19], s8 offen nt
	v_pk_add_f32 v[178:179], v[156:157], v[158:159]
	v_pk_add_f32 v[52:53], v[148:149], v[178:179]
	v_pk_add_f32 v[182:183], v[40:41], v[54:55]
	v_pk_add_f32 v[186:187], v[60:61], v[182:183]
	v_pk_add_f32 v[190:191], v[56:57], v[130:131]
	v_pk_add_f32 v[194:195], v[92:93], v[190:191]
	v_pk_add_f32 v[198:199], v[76:77], v[150:151]
	v_pk_add_f32 v[202:203], v[132:133], v[198:199]
	v_pk_fma_f32 v[186:187], v[144:145], v[52:53], v[186:187] op_sel_hi:[0,1,1] neg_lo:[1,0,0] neg_hi:[1,0,0]
	v_pk_fma_f32 v[194:195], v[144:145], v[52:53], v[194:195] op_sel:[1,0,0] neg_lo:[1,0,0] neg_hi:[1,0,0]
	v_pk_fma_f32 v[202:203], v[146:147], v[52:53], v[202:203] op_sel_hi:[0,1,1] neg_lo:[1,0,0] neg_hi:[1,0,0]
	v_pk_mul_f32 v[40:41], v[146:147], v[186:187] op_sel:[1,0]
	v_pk_mul_f32 v[56:57], v[164:165], v[186:187] op_sel_hi:[0,1]
	v_pk_mul_f32 v[60:61], v[164:165], v[186:187] op_sel:[1,0]
	v_pk_fma_f32 v[40:41], v[164:165], v[194:195], v[40:41] op_sel_hi:[0,1,1]
	v_pk_fma_f32 v[56:57], v[166:167], v[194:195], v[56:57] op_sel_hi:[0,1,1]
	v_pk_fma_f32 v[60:61], v[166:167], v[194:195], v[60:61] op_sel:[1,0,0]
	v_pk_fma_f32 v[40:41], v[164:165], v[202:203], v[40:41] op_sel:[1,0,0]
	v_pk_fma_f32 v[56:57], v[166:167], v[202:203], v[56:57] op_sel:[1,0,0]
	v_pk_fma_f32 v[60:61], v[168:169], v[202:203], v[60:61] op_sel_hi:[0,1,1]
	v_pk_mul_f32 v[206:207], v[144:145], v[40:41] op_sel_hi:[0,1]
	v_pk_fma_f32 v[206:207], v[144:145], v[56:57], v[206:207] op_sel:[1,0,0]
	v_pk_fma_f32 v[206:207], v[146:147], v[60:61], v[206:207] op_sel_hi:[0,1,1]
	v_pk_fma_f32 v[206:207], v[168:169], v[52:53], v[206:207] op_sel:[1,0,0] neg_lo:[0,0,1] neg_hi:[0,0,1]
	v_cmp_eq_u32_e64 s[10:11], 6, v171
	v_cmp_eq_u32_e64 s[14:15], 7, v171
	v_pk_add_f32 v[52:53], v[74:75], v[40:41]
	v_pk_add_f32 v[64:65], v[106:107], v[52:53]
	v_pk_add_f32 v[68:69], v[78:79], v[56:57]
	v_pk_add_f32 v[74:75], v[110:111], v[68:69]
	v_pk_add_f32 v[76:77], v[94:95], v[60:61]
	v_pk_add_f32 v[78:79], v[134:135], v[76:77]
	v_pk_add_f32 v[94:95], v[176:177], v[206:207]
	v_pk_add_f32 v[92:93], v[72:73], v[94:95]
	v_pk_fma_f32 v[72:73], v[116:117], v[64:65], v[92:93] op_sel_hi:[0,1,1]
	v_pk_fma_f32 v[108:109], v[120:121], v[64:65], v[92:93] op_sel_hi:[0,1,1]
	v_pk_fma_f32 v[72:73], v[116:117], v[74:75], v[72:73] op_sel:[1,0,0]
	v_pk_fma_f32 v[108:109], v[120:121], v[74:75], v[108:109] op_sel:[1,0,0]
	v_pk_fma_f32 v[72:73], v[118:119], v[78:79], v[72:73] op_sel_hi:[0,1,1]
	v_pk_fma_f32 v[108:109], v[122:123], v[78:79], v[108:109] op_sel_hi:[0,1,1]
	v_pk_fma_f32 v[92:93], v[32:33], v[64:65], v[92:93] op_sel_hi:[0,1,1]
	v_pk_fma_f32 v[92:93], v[32:33], v[74:75], v[92:93] op_sel:[1,0,0]
	v_pk_fma_f32 v[92:93], v[34:35], v[78:79], v[92:93] op_sel_hi:[0,1,1]
	v_cndmask_b32_e64 v106, 0, v18, s[10:11]
	v_cndmask_b32_e64 v107, 0, v18, s[14:15]
	v_add_f32_dpp v92, v72, v92 wave_shl:1 row_mask:0xf bank_mask:0xf bound_ctrl:1
	v_add_f32_dpp v93, v73, v93 wave_shl:1 row_mask:0xf bank_mask:0xf bound_ctrl:1
	s_add_i32 s4, s34, 0
	s_cmpk_lt_i32 s4, 0x201
	s_cselect_b64 s[12:13], s[0:1], 0
	v_add_f32_dpp v92, v108, v92 wave_shr:1 row_mask:0xf bank_mask:0xf bound_ctrl:1
	v_add_f32_dpp v93, v109, v93 wave_shr:1 row_mask:0xf bank_mask:0xf bound_ctrl:1
	v_pk_fma_f32 v[92:93], v[20:21], v[170:171], v[92:93] op_sel_hi:[1,0,1] neg_lo:[0,0,1] neg_hi:[0,0,1]
	v_pk_add_f32 v[92:93], v[92:93], v[106:107] neg_lo:[0,1] neg_hi:[0,1]
	v_pk_mul_f32 v[110:111], v[92:93], v[92:93]
	v_add_f32_e32 v110, v110, v111
	v_cndmask_b32_e64 v111, 0, v110, s[12:13]
	v_add_f32_e32 v1, v1, v111
	s_waitcnt vmcnt(12)
	v_mov_b32_dpp v32, v112 wave_shr:1 row_mask:0xf bank_mask:0xf bound_ctrl:1
	v_mov_b32_dpp v33, v113 wave_shr:1 row_mask:0xf bank_mask:0xf bound_ctrl:1
	v_mov_b32_dpp v34, v114 wave_shr:1 row_mask:0xf bank_mask:0xf bound_ctrl:1
	v_mov_b32_dpp v72, v112 wave_shl:1 row_mask:0xf bank_mask:0xf bound_ctrl:1
	v_mov_b32_dpp v73, v113 wave_shl:1 row_mask:0xf bank_mask:0xf bound_ctrl:1
	v_mov_b32_dpp v74, v114 wave_shl:1 row_mask:0xf bank_mask:0xf bound_ctrl:1
	s_add_i32 s4, s34, 4
	s_cmpk_lt_u32 s4, 0x201
	s_cselect_b64 s[12:13], s[40:41], 0
	v_cmp_eq_u32_e64 s[14:15], s37, v29
	s_and_b64 s[14:15], s[14:15], s[12:13]
	v_cndmask_b32_e64 v31, 0, 1, s[14:15]
	v_pk_add_f32 v[20:21], v[112:113], v[32:33]
	v_pk_mul_f32 v[64:65], v[112:113], v[112:113] op_sel_hi:[0,1]
	v_or_b32_dpp v43, v31, v31 wave_shr:1 row_mask:0xf bank_mask:0xf bound_ctrl:1
	v_pk_mul_f32 v[78:79], v[112:113], v[114:115] op_sel_hi:[1,0]
	v_or_b32_dpp v43, v31, v43 wave_shl:1 row_mask:0xf bank_mask:0xf bound_ctrl:1
	v_mul_f32_e64 v92, v113, v113
	v_mul_f32_e64 v93, v114, v114
	v_or_b32_dpp v63, v43, v43 wave_shr:1 row_mask:0xf bank_mask:0xf bound_ctrl:1
	v_add_f32_e64 v106, v114, v34
	v_pk_add_f32 v[20:21], v[20:21], v[72:73]
	v_or_b32_dpp v63, v43, v63 wave_shl:1 row_mask:0xf bank_mask:0xf bound_ctrl:1
	v_or3_b32 v31, v63, v44, v45
	v_or3_b32 v31, v31, v62, v96
	s_add_i32 s4, s34, 1
	s_cmpk_lt_u32 s4, 0x1ff
	s_cselect_b64 s[12:13], s[42:43], 0
	v_cmp_ne_u32_e64 s[30:31], 0, v31
	s_and_b64 s[30:31], s[30:31], s[12:13]
	v_cndmask_b32_e64 v31, 0, 1.0, s[30:31]
	v_pk_fma_f32 v[64:65], v[32:33], v[32:33], v[64:65] op_sel_hi:[0,1,1]
	v_pk_fma_f32 v[78:79], v[32:33], v[34:35], v[78:79] op_sel_hi:[1,0,1]
	v_fma_f32 v92, v33, v33, v92
	v_fma_f32 v93, v34, v34, v93
	v_add_f32_dpp v107, v31, v31 wave_shr:1 row_mask:0xf bank_mask:0xf bound_ctrl:1
	v_add_f32_e64 v106, v106, v74
	v_pk_fma_f32 v[64:65], v[72:73], v[72:73], v[64:65] op_sel_hi:[0,1,1]
	v_pk_fma_f32 v[78:79], v[72:73], v[74:75], v[78:79] op_sel_hi:[1,0,1]
	v_fma_f32 v92, v73, v73, v92
	v_fma_f32 v93, v74, v74, v93
	v_add_f32_dpp v107, v31, v107 wave_shl:1 row_mask:0xf bank_mask:0xf bound_ctrl:1
	v_pk_add_f32 v[108:109], v[102:103], v[20:21]
	v_pk_add_f32 v[102:103], v[138:139], v[64:65]
	v_pk_add_f32 v[110:111], v[142:143], v[78:79]
	v_pk_add_f32 v[116:117], v[104:105], v[92:93]
	v_pk_add_f32 v[104:105], v[126:127], v[106:107]
	v_mul_f32_e64 v120, v108, v22
	v_mul_f32_e64 v121, v109, v22
	v_mul_f32_e64 v122, v104, v22
	v_fma_f32 v31, v102, v22, v26
	v_mul_f32_e64 v43, v103, v22
	v_mul_f32_e64 v97, v110, v22
	v_fma_f32 v118, v116, v22, v26
	v_mul_f32_e64 v119, v111, v22
	v_fma_f32 v128, v117, v22, v26
	v_fma_f32 v31, -v120, v120, v31
	v_fma_f32 v43, -v120, v121, v43
	v_fma_f32 v97, -v120, v122, v97
	v_fma_f32 v118, -v121, v121, v118
	v_fma_f32 v119, -v121, v122, v119
	v_fma_f32 v128, -v122, v122, v128
	v_mul_f32_e64 v129, v119, v119
	v_mul_f32_e64 v136, v43, v128
	v_mul_f32_e64 v137, v97, v118
	v_mul_f32_e64 v138, v97, v97
	v_mul_f32_e64 v139, v31, v119
	v_mul_f32_e64 v140, v43, v43
	v_fma_f32 v129, v118, v128, -v129
	v_fma_f32 v136, v97, v119, -v136
	v_fma_f32 v137, v43, v119, -v137
	v_fma_f32 v138, v31, v128, -v138
	v_fma_f32 v139, v43, v97, -v139
	v_fma_f32 v140, v31, v118, -v140
	v_mul_f32_e64 v141, v31, v129
	v_fma_f32 v141, v43, v136, v141
	v_fma_f32 v141, v97, v137, v141
	v_rcp_f32_e32 v141, v141
	v_cmp_ne_u32_e64 vcc, s37, v17
	v_mul_f32_e64 v141, v141, v22
	v_cndmask_b32_e64 v141, 0, v141, s[30:31]
	v_cndmask_b32_e64 v31, 0, v18, vcc
	v_cndmask_b32_e64 v133, 0, v22, s[30:31]
	v_mul_f32_e64 v123, v129, v141
	v_mul_f32_e64 v124, v136, v141
	v_mul_f32_e64 v125, v137, v141
	v_mul_f32_e64 v126, v138, v141
	v_mul_f32_e64 v127, v139, v141
	v_mul_f32_e64 v132, v140, v141
	v_add_f32_e64 v134, v105, v31
	v_mov_b32_e32 v135, v17
	ds_write_b128 v23, v[120:123] offset:3072
	ds_write_b128 v23, v[124:127] offset:4096
	ds_write_b128 v23, v[132:135] offset:5120
	v_mov_b32_dpp v102, v100 wave_shr:1 row_mask:0xf bank_mask:0xf bound_ctrl:1
	v_mov_b32_dpp v103, v101 wave_shr:1 row_mask:0xf bank_mask:0xf bound_ctrl:1
	v_mov_b32_dpp v110, v100 wave_shl:1 row_mask:0xf bank_mask:0xf bound_ctrl:1
	v_mov_b32_dpp v111, v101 wave_shl:1 row_mask:0xf bank_mask:0xf bound_ctrl:1
	v_pk_mul_f32 v[96:97], v[100:101], v[112:113] op_sel_hi:[1,0]
	v_pk_mul_f32 v[104:105], v[100:101], v[112:113] op_sel:[0,1]
	v_pk_mul_f32 v[108:109], v[100:101], v[114:115] op_sel_hi:[1,0]
	v_pk_add_f32 v[116:117], v[100:101], v[102:103]
	v_pk_fma_f32 v[96:97], v[102:103], v[32:33], v[96:97] op_sel_hi:[1,0,1]
	v_pk_fma_f32 v[104:105], v[102:103], v[32:33], v[104:105] op_sel:[0,1,0]
	v_pk_fma_f32 v[108:109], v[102:103], v[34:35], v[108:109] op_sel_hi:[1,0,1]
	v_pk_add_f32 v[116:117], v[116:117], v[110:111]
	v_pk_fma_f32 v[96:97], v[110:111], v[72:73], v[96:97] op_sel_hi:[1,0,1]
	v_pk_fma_f32 v[104:105], v[110:111], v[72:73], v[104:105] op_sel:[0,1,0]
	v_pk_fma_f32 v[108:109], v[110:111], v[74:75], v[108:109] op_sel_hi:[1,0,1]
	s_waitcnt lgkmcnt(0)
	s_barrier
	s_add_i32 s5, s34, 7
	s_min_i32 s5, s5, 0x200
	s_mul_i32 s6, s5, 0x804
	s_add_i32 s6, s6, s35
	s_add_i32 s7, s6, 0x505014
	s_add_i32 s8, s6, 0x606018
	s_mul_i32 s9, s5, 0x180c
	s_add_i32 s9, s9, s33
	s_add_i32 s4, s34, 8
	s_min_i32 s4, s4, 0x200
	s_mul_i32 s4, s4, 0x804
	s_add_i32 s4, s4, s38
	buffer_load_dword v17, v28, s[20:23], s4 offen nt
	buffer_load_dwordx3 v[136:138], v27, s[24:27], s9 offen nt
	buffer_load_dword v102, v28, s[16:19], s7 offen nt
	buffer_load_dword v103, v28, s[16:19], s8 offen nt
	v_pk_add_f32 v[110:111], v[178:179], v[116:117]
	v_pk_add_f32 v[128:129], v[182:183], v[96:97]
	v_pk_add_f32 v[140:141], v[190:191], v[104:105]
	v_pk_add_f32 v[144:145], v[198:199], v[108:109]
	v_pk_fma_f32 v[128:129], v[120:121], v[110:111], v[128:129] op_sel_hi:[0,1,1] neg_lo:[1,0,0] neg_hi:[1,0,0]
	v_pk_fma_f32 v[140:141], v[120:121], v[110:111], v[140:141] op_sel:[1,0,0] neg_lo:[1,0,0] neg_hi:[1,0,0]
	v_pk_fma_f32 v[144:145], v[122:123], v[110:111], v[144:145] op_sel_hi:[0,1,1] neg_lo:[1,0,0] neg_hi:[1,0,0]
	v_pk_mul_f32 v[118:119], v[122:123], v[128:129] op_sel:[1,0]
	v_pk_mul_f32 v[142:143], v[124:125], v[128:129] op_sel_hi:[0,1]
	v_pk_mul_f32 v[146:147], v[124:125], v[128:129] op_sel:[1,0]
	v_pk_fma_f32 v[118:119], v[124:125], v[140:141], v[118:119] op_sel_hi:[0,1,1]
	v_pk_fma_f32 v[142:143], v[126:127], v[140:141], v[142:143] op_sel_hi:[0,1,1]
	v_pk_fma_f32 v[146:147], v[126:127], v[140:141], v[146:147] op_sel:[1,0,0]
	v_pk_fma_f32 v[118:119], v[124:125], v[144:145], v[118:119] op_sel:[1,0,0]
	v_pk_fma_f32 v[142:143], v[126:127], v[144:145], v[142:143] op_sel:[1,0,0]
	v_pk_fma_f32 v[146:147], v[132:133], v[144:145], v[146:147] op_sel_hi:[0,1,1]
	v_pk_mul_f32 v[148:149], v[120:121], v[118:119] op_sel_hi:[0,1]
	v_pk_fma_f32 v[148:149], v[120:121], v[142:143], v[148:149] op_sel:[1,0,0]
	v_pk_fma_f32 v[148:149], v[122:123], v[146:147], v[148:149] op_sel_hi:[0,1,1]
	v_pk_fma_f32 v[148:149], v[132:133], v[110:111], v[148:149] op_sel:[1,0,0] neg_lo:[0,0,1] neg_hi:[0,0,1]
	v_cmp_eq_u32_e64 s[10:11], 6, v135
	v_cmp_eq_u32_e64 s[14:15], 7, v135
	v_pk_add_f32 v[110:111], v[52:53], v[118:119]
	v_pk_add_f32 v[52:53], v[68:69], v[142:143]
	v_pk_add_f32 v[68:69], v[76:77], v[146:147]
	v_pk_add_f32 v[166:167], v[94:95], v[148:149]
	v_pk_fma_f32 v[94:95], v[8:9], v[110:111], v[166:167] op_sel_hi:[0,1,1]
	v_pk_fma_f32 v[170:171], v[48:49], v[110:111], v[166:167] op_sel_hi:[0,1,1]
	v_pk_fma_f32 v[94:95], v[8:9], v[52:53], v[94:95] op_sel:[1,0,0]
	v_pk_fma_f32 v[170:171], v[48:49], v[52:53], v[170:171] op_sel:[1,0,0]
	v_pk_fma_f32 v[94:95], v[10:11], v[68:69], v[94:95] op_sel_hi:[0,1,1]
	v_pk_fma_f32 v[170:171], v[50:51], v[68:69], v[170:171] op_sel_hi:[0,1,1]
	v_pk_fma_f32 v[166:167], v[36:37], v[110:111], v[166:167] op_sel_hi:[0,1,1]
	v_pk_fma_f32 v[166:167], v[36:37], v[52:53], v[166:167] op_sel:[1,0,0]
	v_pk_fma_f32 v[166:167], v[38:39], v[68:69], v[166:167] op_sel_hi:[0,1,1]
	v_cndmask_b32_e64 v76, 0, v18, s[10:11]
	v_cndmask_b32_e64 v77, 0, v18, s[14:15]
	v_add_f32_dpp v166, v94, v166 wave_shl:1 row_mask:0xf bank_mask:0xf bound_ctrl:1
	v_add_f32_dpp v167, v95, v167 wave_shl:1 row_mask:0xf bank_mask:0xf bound_ctrl:1
	s_add_i32 s4, s34, 1
	s_cmpk_lt_i32 s4, 0x201
	s_cselect_b64 s[12:13], s[0:1], 0
	v_add_f32_dpp v166, v170, v166 wave_shr:1 row_mask:0xf bank_mask:0xf bound_ctrl:1
	v_add_f32_dpp v167, v171, v167 wave_shr:1 row_mask:0xf bank_mask:0xf bound_ctrl:1
	v_pk_fma_f32 v[166:167], v[24:25], v[134:135], v[166:167] op_sel_hi:[1,0,1] neg_lo:[0,0,1] neg_hi:[0,0,1]
	v_pk_add_f32 v[166:167], v[166:167], v[76:77] neg_lo:[0,1] neg_hi:[0,1]
	v_pk_mul_f32 v[128:129], v[166:167], v[166:167]
	v_add_f32_e32 v128, v128, v129
	v_cndmask_b32_e64 v129, 0, v128, s[12:13]
	v_add_f32_e32 v1, v1, v129
	s_waitcnt vmcnt(12)
	v_mov_b32_dpp v8, v152 wave_shr:1 row_mask:0xf bank_mask:0xf bound_ctrl:1
	v_mov_b32_dpp v9, v153 wave_shr:1 row_mask:0xf bank_mask:0xf bound_ctrl:1
	v_mov_b32_dpp v10, v154 wave_shr:1 row_mask:0xf bank_mask:0xf bound_ctrl:1
	v_mov_b32_dpp v36, v152 wave_shl:1 row_mask:0xf bank_mask:0xf bound_ctrl:1
	v_mov_b32_dpp v37, v153 wave_shl:1 row_mask:0xf bank_mask:0xf bound_ctrl:1
	v_mov_b32_dpp v38, v154 wave_shl:1 row_mask:0xf bank_mask:0xf bound_ctrl:1
	s_add_i32 s4, s34, 5
	s_cmpk_lt_u32 s4, 0x201
	s_cselect_b64 s[12:13], s[40:41], 0
	v_cmp_eq_u32_e64 s[14:15], s37, v2
	s_and_b64 s[14:15], s[14:15], s[12:13]
	v_cndmask_b32_e64 v31, 0, 1, s[14:15]
	v_pk_add_f32 v[24:25], v[152:153], v[8:9]
	v_pk_mul_f32 v[48:49], v[152:153], v[152:153] op_sel_hi:[0,1]
	v_or_b32_dpp v43, v31, v31 wave_shr:1 row_mask:0xf bank_mask:0xf bound_ctrl:1
	v_pk_mul_f32 v[50:51], v[152:153], v[154:155] op_sel_hi:[1,0]
	v_or_b32_dpp v43, v31, v43 wave_shl:1 row_mask:0xf bank_mask:0xf bound_ctrl:1
	v_mul_f32_e64 v52, v153, v153
	v_mul_f32_e64 v53, v154, v154
	v_or_b32_dpp v76, v43, v43 wave_shr:1 row_mask:0xf bank_mask:0xf bound_ctrl:1
	v_add_f32_e64 v68, v154, v10
	v_pk_add_f32 v[24:25], v[24:25], v[36:37]
	v_or_b32_dpp v76, v43, v76 wave_shl:1 row_mask:0xf bank_mask:0xf bound_ctrl:1
	v_or3_b32 v31, v76, v63, v44
	v_or3_b32 v31, v31, v45, v62
	s_add_i32 s4, s34, 2
	s_cmpk_lt_u32 s4, 0x1ff
	s_cselect_b64 s[12:13], s[42:43], 0
	v_cmp_ne_u32_e64 s[30:31], 0, v31
	s_and_b64 s[30:31], s[30:31], s[12:13]
	v_cndmask_b32_e64 v31, 0, 1.0, s[30:31]
	v_pk_fma_f32 v[48:49], v[8:9], v[8:9], v[48:49] op_sel_hi:[0,1,1]
	v_pk_fma_f32 v[50:51], v[8:9], v[10:11], v[50:51] op_sel_hi:[1,0,1]
	v_fma_f32 v52, v9, v9, v52
	v_fma_f32 v53, v10, v10, v53
	v_add_f32_dpp v69, v31, v31 wave_shr:1 row_mask:0xf bank_mask:0xf bound_ctrl:1
	v_add_f32_e64 v68, v68, v38
	v_pk_fma_f32 v[48:49], v[36:37], v[36:37], v[48:49] op_sel_hi:[0,1,1]
	v_pk_fma_f32 v[50:51], v[36:37], v[38:39], v[50:51] op_sel_hi:[1,0,1]
	v_fma_f32 v52, v37, v37, v52
	v_fma_f32 v53, v38, v38, v53
	v_add_f32_dpp v69, v31, v69 wave_shl:1 row_mask:0xf bank_mask:0xf bound_ctrl:1
	v_pk_add_f32 v[120:121], v[20:21], v[24:25]
	v_pk_add_f32 v[94:95], v[6:7], v[120:121]
	v_pk_add_f32 v[20:21], v[64:65], v[48:49]
	v_pk_add_f32 v[6:7], v[58:59], v[20:21]
	v_pk_add_f32 v[58:59], v[78:79], v[50:51]
	v_pk_add_f32 v[64:65], v[88:89], v[58:59]
	v_pk_add_f32 v[88:89], v[92:93], v[52:53]
	v_pk_add_f32 v[78:79], v[90:91], v[88:89]
	v_pk_add_f32 v[92:93], v[106:107], v[68:69]
	v_pk_add_f32 v[90:91], v[98:99], v[92:93]
	v_mul_f32_e64 v124, v94, v22
	v_mul_f32_e64 v125, v95, v22
	v_mul_f32_e64 v126, v90, v22
	v_fma_f32 v31, v6, v22, v26
	v_mul_f32_e64 v43, v7, v22
	v_mul_f32_e64 v77, v64, v22
	v_fma_f32 v98, v78, v22, v26
	v_mul_f32_e64 v99, v65, v22
	v_fma_f32 v106, v79, v22, v26
	v_fma_f32 v31, -v124, v124, v31
	v_fma_f32 v43, -v124, v125, v43
	v_fma_f32 v77, -v124, v126, v77
	v_fma_f32 v98, -v125, v125, v98
	v_fma_f32 v99, -v125, v126, v99
	v_fma_f32 v106, -v126, v126, v106
	v_mul_f32_e64 v107, v99, v99
	v_mul_f32_e64 v110, v43, v106
	v_mul_f32_e64 v111, v77, v98
	v_mul_f32_e64 v122, v77, v77
	v_mul_f32_e64 v123, v31, v99
	v_mul_f32_e64 v128, v43, v43
	v_fma_f32 v107, v98, v106, -v107
	v_fma_f32 v110, v77, v99, -v110
	v_fma_f32 v111, v43, v99, -v111
	v_fma_f32 v122, v31, v106, -v122
	v_fma_f32 v123, v43, v77, -v123
	v_fma_f32 v128, v31, v98, -v128
	v_mul_f32_e64 v129, v31, v107
	v_fma_f32 v129, v43, v110, v129
	v_fma_f32 v129, v77, v111, v129
	v_rcp_f32_e32 v129, v129
	v_cmp_ne_u32_e64 vcc, s37, v30
	v_mul_f32_e64 v129, v129, v22
	v_cndmask_b32_e64 v129, 0, v129, s[30:31]
	v_cndmask_b32_e64 v31, 0, v18, vcc
	v_cndmask_b32_e64 v165, 0, v22, s[30:31]
	v_mul_f32_e64 v127, v107, v129
	v_mul_f32_e64 v132, v110, v129
	v_mul_f32_e64 v133, v111, v129
	v_mul_f32_e64 v134, v122, v129
	v_mul_f32_e64 v135, v123, v129
	v_mul_f32_e64 v164, v128, v129
	v_add_f32_e64 v166, v91, v31
	v_mov_b32_e32 v167, v30
	ds_write_b128 v23, v[124:127]
	ds_write_b128 v23, v[132:135] offset:1024
	ds_write_b128 v23, v[164:167] offset:2048
	v_mov_b32_dpp v64, v70 wave_shr:1 row_mask:0xf bank_mask:0xf bound_ctrl:1
	v_mov_b32_dpp v65, v71 wave_shr:1 row_mask:0xf bank_mask:0xf bound_ctrl:1
	v_mov_b32_dpp v128, v70 wave_shl:1 row_mask:0xf bank_mask:0xf bound_ctrl:1
	v_mov_b32_dpp v129, v71 wave_shl:1 row_mask:0xf bank_mask:0xf bound_ctrl:1
	v_pk_mul_f32 v[6:7], v[70:71], v[152:153] op_sel_hi:[1,0]
	v_pk_mul_f32 v[30:31], v[70:71], v[152:153] op_sel:[0,1]
	v_pk_mul_f32 v[78:79], v[70:71], v[154:155] op_sel_hi:[1,0]
	v_pk_add_f32 v[90:91], v[70:71], v[64:65]
	v_pk_fma_f32 v[6:7], v[64:65], v[8:9], v[6:7] op_sel_hi:[1,0,1]
	v_pk_fma_f32 v[30:31], v[64:65], v[8:9], v[30:31] op_sel:[0,1,0]
	v_pk_fma_f32 v[78:79], v[64:65], v[10:11], v[78:79] op_sel_hi:[1,0,1]
	v_pk_add_f32 v[90:91], v[90:91], v[128:129]
	v_pk_fma_f32 v[6:7], v[128:129], v[36:37], v[6:7] op_sel_hi:[1,0,1]
	v_pk_fma_f32 v[30:31], v[128:129], v[36:37], v[30:31] op_sel:[0,1,0]
	v_pk_fma_f32 v[78:79], v[128:129], v[38:39], v[78:79] op_sel_hi:[1,0,1]
	s_waitcnt lgkmcnt(0)
	s_barrier
	s_add_i32 s5, s34, 8
	s_min_i32 s5, s5, 0x200
	s_mul_i32 s6, s5, 0x804
	s_add_i32 s6, s6, s35
	s_add_i32 s7, s6, 0x505014
	s_add_i32 s8, s6, 0x606018
	s_mul_i32 s9, s5, 0x180c
	s_add_i32 s9, s9, s33
	s_add_i32 s4, s34, 9
	s_min_i32 s4, s4, 0x200
	s_mul_i32 s4, s4, 0x804
	s_add_i32 s4, s4, s38
	buffer_load_dword v43, v28, s[20:23], s4 offen nt
	buffer_load_dwordx3 v[168:170], v27, s[24:27], s9 offen nt
	buffer_load_dword v64, v28, s[16:19], s7 offen nt
	buffer_load_dword v65, v28, s[16:19], s8 offen nt
	v_pk_add_f32 v[128:129], v[116:117], v[90:91]
	v_pk_add_f32 v[94:95], v[158:159], v[128:129]
	v_pk_add_f32 v[116:117], v[96:97], v[6:7]
	v_pk_add_f32 v[140:141], v[54:55], v[116:117]
	v_pk_add_f32 v[96:97], v[104:105], v[30:31]
	v_pk_add_f32 v[144:145], v[130:131], v[96:97]
	v_pk_add_f32 v[104:105], v[108:109], v[78:79]
	v_pk_add_f32 v[156:157], v[150:151], v[104:105]
	v_pk_fma_f32 v[140:141], v[124:125], v[94:95], v[140:141] op_sel_hi:[0,1,1] neg_lo:[1,0,0] neg_hi:[1,0,0]
	v_pk_fma_f32 v[144:145], v[124:125], v[94:95], v[144:145] op_sel:[1,0,0] neg_lo:[1,0,0] neg_hi:[1,0,0]
	v_pk_fma_f32 v[156:157], v[126:127], v[94:95], v[156:157] op_sel_hi:[0,1,1] neg_lo:[1,0,0] neg_hi:[1,0,0]
	v_pk_mul_f32 v[54:55], v[126:127], v[140:141] op_sel:[1,0]
	v_pk_mul_f32 v[98:99], v[132:133], v[140:141] op_sel_hi:[0,1]
	v_pk_mul_f32 v[106:107], v[132:133], v[140:141] op_sel:[1,0]
	v_pk_fma_f32 v[54:55], v[132:133], v[144:145], v[54:55] op_sel_hi:[0,1,1]
	v_pk_fma_f32 v[98:99], v[134:135], v[144:145], v[98:99] op_sel_hi:[0,1,1]
	v_pk_fma_f32 v[106:107], v[134:135], v[144:145], v[106:107] op_sel:[1,0,0]
	v_pk_fma_f32 v[54:55], v[132:133], v[156:157], v[54:55] op_sel:[1,0,0]
	v_pk_fma_f32 v[98:99], v[134:135], v[156:157], v[98:99] op_sel:[1,0,0]
	v_pk_fma_f32 v[106:107], v[164:165], v[156:157], v[106:107] op_sel_hi:[0,1,1]
	v_pk_mul_f32 v[108:109], v[124:125], v[54:55] op_sel_hi:[0,1]
	v_pk_fma_f32 v[108:109], v[124:125], v[98:99], v[108:109] op_sel:[1,0,0]
	v_pk_fma_f32 v[108:109], v[126:127], v[106:107], v[108:109] op_sel_hi:[0,1,1]
	v_pk_fma_f32 v[108:109], v[164:165], v[94:95], v[108:109] op_sel:[1,0,0] neg_lo:[0,0,1] neg_hi:[0,0,1]
	v_cmp_eq_u32_e64 s[10:11], 6, v167
	v_cmp_eq_u32_e64 s[14:15], 7, v167
	v_pk_add_f32 v[94:95], v[118:119], v[54:55]
	v_pk_add_f32 v[110:111], v[40:41], v[94:95]
	v_pk_add_f32 v[118:119], v[142:143], v[98:99]
	v_pk_add_f32 v[40:41], v[56:57], v[118:119]
	v_pk_add_f32 v[122:123], v[146:147], v[106:107]
	v_pk_add_f32 v[56:57], v[60:61], v[122:123]
	v_pk_add_f32 v[60:61], v[148:149], v[108:109]
	v_pk_add_f32 v[130:131], v[206:207], v[60:61]
	v_pk_fma_f32 v[142:143], v[12:13], v[110:111], v[130:131] op_sel_hi:[0,1,1]
	v_pk_fma_f32 v[146:147], v[84:85], v[110:111], v[130:131] op_sel_hi:[0,1,1]
	v_pk_fma_f32 v[142:143], v[12:13], v[40:41], v[142:143] op_sel:[1,0,0]
	v_pk_fma_f32 v[146:147], v[84:85], v[40:41], v[146:147] op_sel:[1,0,0]
	v_pk_fma_f32 v[142:143], v[14:15], v[56:57], v[142:143] op_sel_hi:[0,1,1]
	v_pk_fma_f32 v[146:147], v[86:87], v[56:57], v[146:147] op_sel_hi:[0,1,1]
	v_pk_fma_f32 v[130:131], v[80:81], v[110:111], v[130:131] op_sel_hi:[0,1,1]
	v_pk_fma_f32 v[130:131], v[80:81], v[40:41], v[130:131] op_sel:[1,0,0]
	v_pk_fma_f32 v[130:131], v[82:83], v[56:57], v[130:131] op_sel_hi:[0,1,1]
	v_cndmask_b32_e64 v140, 0, v18, s[10:11]
	v_cndmask_b32_e64 v141, 0, v18, s[14:15]
	v_add_f32_dpp v130, v142, v130 wave_shl:1 row_mask:0xf bank_mask:0xf bound_ctrl:1
	v_add_f32_dpp v131, v143, v131 wave_shl:1 row_mask:0xf bank_mask:0xf bound_ctrl:1
	s_add_i32 s4, s34, 2
	s_cmpk_lt_i32 s4, 0x201
	s_cselect_b64 s[12:13], s[0:1], 0
	v_add_f32_dpp v130, v146, v130 wave_shr:1 row_mask:0xf bank_mask:0xf bound_ctrl:1
	v_add_f32_dpp v131, v147, v131 wave_shr:1 row_mask:0xf bank_mask:0xf bound_ctrl:1
	v_pk_fma_f32 v[130:131], v[66:67], v[166:167], v[130:131] op_sel_hi:[1,0,1] neg_lo:[0,0,1] neg_hi:[0,0,1]
	v_pk_add_f32 v[130:131], v[130:131], v[140:141] neg_lo:[0,1] neg_hi:[0,1]
	v_pk_mul_f32 v[144:145], v[130:131], v[130:131]
	v_add_f32_e32 v144, v144, v145
	v_cndmask_b32_e64 v145, 0, v144, s[12:13]
	v_add_f32_e32 v1, v1, v145
	s_waitcnt vmcnt(12)
	v_mov_b32_dpp v12, v160 wave_shr:1 row_mask:0xf bank_mask:0xf bound_ctrl:1
	v_mov_b32_dpp v13, v161 wave_shr:1 row_mask:0xf bank_mask:0xf bound_ctrl:1
	v_mov_b32_dpp v14, v162 wave_shr:1 row_mask:0xf bank_mask:0xf bound_ctrl:1
	v_mov_b32_dpp v80, v160 wave_shl:1 row_mask:0xf bank_mask:0xf bound_ctrl:1
	v_mov_b32_dpp v81, v161 wave_shl:1 row_mask:0xf bank_mask:0xf bound_ctrl:1
	v_mov_b32_dpp v82, v162 wave_shl:1 row_mask:0xf bank_mask:0xf bound_ctrl:1
	s_add_i32 s4, s34, 6
	s_cmpk_lt_u32 s4, 0x201
	s_cselect_b64 s[12:13], s[40:41], 0
	v_cmp_eq_u32_e64 s[14:15], s37, v3
	s_and_b64 s[14:15], s[14:15], s[12:13]
	v_cndmask_b32_e64 v62, 0, 1, s[14:15]
	v_pk_add_f32 v[40:41], v[160:161], v[12:13]
	v_pk_mul_f32 v[56:57], v[160:161], v[160:161] op_sel_hi:[0,1]
	v_or_b32_dpp v77, v62, v62 wave_shr:1 row_mask:0xf bank_mask:0xf bound_ctrl:1
	v_pk_mul_f32 v[66:67], v[160:161], v[162:163] op_sel_hi:[1,0]
	v_or_b32_dpp v77, v62, v77 wave_shl:1 row_mask:0xf bank_mask:0xf bound_ctrl:1
	v_mul_f32_e64 v84, v161, v161
	v_mul_f32_e64 v85, v162, v162
	v_or_b32_dpp v110, v77, v77 wave_shr:1 row_mask:0xf bank_mask:0xf bound_ctrl:1
	v_add_f32_e64 v86, v162, v14
	v_pk_add_f32 v[40:41], v[40:41], v[80:81]
	v_or_b32_dpp v110, v77, v110 wave_shl:1 row_mask:0xf bank_mask:0xf bound_ctrl:1
	v_or3_b32 v62, v110, v76, v63
	v_or3_b32 v62, v62, v44, v45
	s_add_i32 s4, s34, 3
	s_cmpk_lt_u32 s4, 0x1ff
	s_cselect_b64 s[12:13], s[42:43], 0
	v_cmp_ne_u32_e64 s[30:31], 0, v62
	s_and_b64 s[30:31], s[30:31], s[12:13]
	v_cndmask_b32_e64 v62, 0, 1.0, s[30:31]
	v_pk_fma_f32 v[56:57], v[12:13], v[12:13], v[56:57] op_sel_hi:[0,1,1]
	v_pk_fma_f32 v[66:67], v[12:13], v[14:15], v[66:67] op_sel_hi:[1,0,1]
	v_fma_f32 v84, v13, v13, v84
	v_fma_f32 v85, v14, v14, v85
	v_add_f32_dpp v87, v62, v62 wave_shr:1 row_mask:0xf bank_mask:0xf bound_ctrl:1
	v_add_f32_e64 v86, v86, v82
	v_pk_fma_f32 v[56:57], v[80:81], v[80:81], v[56:57] op_sel_hi:[0,1,1]
	v_pk_fma_f32 v[66:67], v[80:81], v[82:83], v[66:67] op_sel_hi:[1,0,1]
	v_fma_f32 v84, v81, v81, v84
	v_fma_f32 v85, v82, v82, v85
	v_add_f32_dpp v87, v62, v87 wave_shl:1 row_mask:0xf bank_mask:0xf bound_ctrl:1
	v_pk_add_f32 v[124:125], v[120:121], v[40:41]
	v_pk_add_f32 v[120:121], v[20:21], v[56:57]
	v_pk_add_f32 v[20:21], v[58:59], v[66:67]
	v_pk_add_f32 v[58:59], v[88:89], v[84:85]
	v_pk_add_f32 v[88:89], v[92:93], v[86:87]
	v_mul_f32_e64 v132, v124, v22
	v_mul_f32_e64 v133, v125, v22
	v_mul_f32_e64 v134, v88, v22
	v_fma_f32 v62, v120, v22, v26
	v_mul_f32_e64 v77, v121, v22
	v_mul_f32_e64 v111, v20, v22
	v_fma_f32 v92, v58, v22, v26
	v_mul_f32_e64 v93, v21, v22
	v_fma_f32 v126, v59, v22, v26
	v_fma_f32 v62, -v132, v132, v62
	v_fma_f32 v77, -v132, v133, v77
	v_fma_f32 v111, -v132, v134, v111
	v_fma_f32 v92, -v133, v133, v92
	v_fma_f32 v93, -v133, v134, v93
	v_fma_f32 v126, -v134, v134, v126
	v_mul_f32_e64 v127, v93, v93
	v_mul_f32_e64 v130, v77, v126
	v_mul_f32_e64 v131, v111, v92
	v_mul_f32_e64 v148, v111, v111
	v_mul_f32_e64 v149, v62, v93
	v_mul_f32_e64 v150, v77, v77
	v_fma_f32 v127, v92, v126, -v127
	v_fma_f32 v130, v111, v93, -v130
	v_fma_f32 v131, v77, v93, -v131
	v_fma_f32 v148, v62, v126, -v148
	v_fma_f32 v149, v77, v111, -v149
	v_fma_f32 v150, v62, v92, -v150
	v_mul_f32_e64 v151, v62, v127
	v_fma_f32 v151, v77, v130, v151
	v_fma_f32 v151, v111, v131, v151
	v_rcp_f32_e32 v151, v151
	v_cmp_ne_u32_e64 vcc, s37, v42
	v_mul_f32_e64 v151, v151, v22
	v_cndmask_b32_e64 v151, 0, v151, s[30:31]
	v_cndmask_b32_e64 v62, 0, v18, vcc
	v_cndmask_b32_e64 v145, 0, v22, s[30:31]
	v_mul_f32_e64 v135, v127, v151
	v_mul_f32_e64 v140, v130, v151
	v_mul_f32_e64 v141, v131, v151
	v_mul_f32_e64 v142, v148, v151
	v_mul_f32_e64 v143, v149, v151
	v_mul_f32_e64 v144, v150, v151
	v_add_f32_e64 v146, v89, v62
	v_mov_b32_e32 v147, v42
	ds_write_b128 v23, v[132:135] offset:3072
	ds_write_b128 v23, v[140:143] offset:4096
	ds_write_b128 v23, v[144:147] offset:5120
	v_mov_b32_dpp v20, v46 wave_shr:1 row_mask:0xf bank_mask:0xf bound_ctrl:1
	v_mov_b32_dpp v21, v47 wave_shr:1 row_mask:0xf bank_mask:0xf bound_ctrl:1
	v_mov_b32_dpp v88, v46 wave_shl:1 row_mask:0xf bank_mask:0xf bound_ctrl:1
	v_mov_b32_dpp v89, v47 wave_shl:1 row_mask:0xf bank_mask:0xf bound_ctrl:1
	v_pk_mul_f32 v[58:59], v[46:47], v[160:161] op_sel_hi:[1,0]
	v_pk_mul_f32 v[126:127], v[46:47], v[160:161] op_sel:[0,1]
	v_pk_mul_f32 v[130:131], v[46:47], v[162:163] op_sel_hi:[1,0]
	v_pk_add_f32 v[150:151], v[46:47], v[20:21]
	v_pk_fma_f32 v[58:59], v[20:21], v[12:13], v[58:59] op_sel_hi:[1,0,1]
	v_pk_fma_f32 v[126:127], v[20:21], v[12:13], v[126:127] op_sel:[0,1,0]
	v_pk_fma_f32 v[130:131], v[20:21], v[14:15], v[130:131] op_sel_hi:[1,0,1]
	v_pk_add_f32 v[150:151], v[150:151], v[88:89]
	v_pk_fma_f32 v[58:59], v[88:89], v[80:81], v[58:59] op_sel_hi:[1,0,1]
	v_pk_fma_f32 v[126:127], v[88:89], v[80:81], v[126:127] op_sel:[0,1,0]
	v_pk_fma_f32 v[130:131], v[88:89], v[82:83], v[130:131] op_sel_hi:[1,0,1]
	s_waitcnt lgkmcnt(0)
	s_barrier
	s_add_i32 s5, s34, 9
	s_min_i32 s5, s5, 0x200
	s_mul_i32 s6, s5, 0x804
	s_add_i32 s6, s6, s35
	s_add_i32 s7, s6, 0x505014
	s_add_i32 s8, s6, 0x606018
	s_mul_i32 s9, s5, 0x180c
	s_add_i32 s9, s9, s33
	s_add_i32 s4, s34, 10
	s_min_i32 s4, s4, 0x200
	s_mul_i32 s4, s4, 0x804
	s_add_i32 s4, s4, s38
	buffer_load_dword v42, v28, s[20:23], s4 offen nt
	buffer_load_dwordx3 v[156:158], v27, s[24:27], s9 offen nt
	buffer_load_dword v20, v28, s[16:19], s7 offen nt
	buffer_load_dword v21, v28, s[16:19], s8 offen nt
	v_pk_add_f32 v[88:89], v[128:129], v[150:151]
	v_pk_add_f32 v[166:167], v[116:117], v[58:59]
	v_pk_add_f32 v[178:179], v[96:97], v[126:127]
	v_pk_add_f32 v[182:183], v[104:105], v[130:131]
	v_pk_fma_f32 v[166:167], v[132:133], v[88:89], v[166:167] op_sel_hi:[0,1,1] neg_lo:[1,0,0] neg_hi:[1,0,0]
	v_pk_fma_f32 v[178:179], v[132:133], v[88:89], v[178:179] op_sel:[1,0,0] neg_lo:[1,0,0] neg_hi:[1,0,0]
	v_pk_fma_f32 v[182:183], v[134:135], v[88:89], v[182:183] op_sel_hi:[0,1,1] neg_lo:[1,0,0] neg_hi:[1,0,0]
	v_pk_mul_f32 v[92:93], v[134:135], v[166:167] op_sel:[1,0]
	v_pk_mul_f32 v[96:97], v[140:141], v[166:167] op_sel_hi:[0,1]
	v_pk_mul_f32 v[104:105], v[140:141], v[166:167] op_sel:[1,0]
	v_pk_fma_f32 v[92:93], v[140:141], v[178:179], v[92:93] op_sel_hi:[0,1,1]
	v_pk_fma_f32 v[96:97], v[142:143], v[178:179], v[96:97] op_sel_hi:[0,1,1]
	v_pk_fma_f32 v[104:105], v[142:143], v[178:179], v[104:105] op_sel:[1,0,0]
	v_pk_fma_f32 v[92:93], v[140:141], v[182:183], v[92:93] op_sel:[1,0,0]
	v_pk_fma_f32 v[96:97], v[142:143], v[182:183], v[96:97] op_sel:[1,0,0]
	v_pk_fma_f32 v[104:105], v[144:145], v[182:183], v[104:105] op_sel_hi:[0,1,1]
	v_pk_mul_f32 v[186:187], v[132:133], v[92:93] op_sel_hi:[0,1]
	v_pk_fma_f32 v[186:187], v[132:133], v[96:97], v[186:187] op_sel:[1,0,0]
	v_pk_fma_f32 v[186:187], v[134:135], v[104:105], v[186:187] op_sel_hi:[0,1,1]
	v_pk_fma_f32 v[186:187], v[144:145], v[88:89], v[186:187] op_sel:[1,0,0] neg_lo:[0,0,1] neg_hi:[0,0,1]
	v_cmp_eq_u32_e64 s[10:11], 6, v147
	v_cmp_eq_u32_e64 s[14:15], 7, v147
	v_pk_add_f32 v[88:89], v[94:95], v[92:93]
	v_pk_add_f32 v[94:95], v[118:119], v[96:97]
	v_pk_add_f32 v[116:117], v[122:123], v[104:105]
	v_pk_add_f32 v[118:119], v[60:61], v[186:187]
	v_pk_fma_f32 v[122:123], v[32:33], v[88:89], v[118:119] op_sel_hi:[0,1,1]
	v_pk_fma_f32 v[166:167], v[72:73], v[88:89], v[118:119] op_sel_hi:[0,1,1]
	v_pk_fma_f32 v[122:123], v[32:33], v[94:95], v[122:123] op_sel:[1,0,0]
	v_pk_fma_f32 v[166:167], v[72:73], v[94:95], v[166:167] op_sel:[1,0,0]
	v_pk_fma_f32 v[122:123], v[34:35], v[116:117], v[122:123] op_sel_hi:[0,1,1]
	v_pk_fma_f32 v[166:167], v[74:75], v[116:117], v[166:167] op_sel_hi:[0,1,1]
	v_pk_fma_f32 v[118:119], v[112:113], v[88:89], v[118:119] op_sel_hi:[0,1,1]
	v_pk_fma_f32 v[118:119], v[112:113], v[94:95], v[118:119] op_sel:[1,0,0]
	v_pk_fma_f32 v[118:119], v[114:115], v[116:117], v[118:119] op_sel_hi:[0,1,1]
	v_cndmask_b32_e64 v60, 0, v18, s[10:11]
	v_cndmask_b32_e64 v61, 0, v18, s[14:15]
	v_add_f32_dpp v118, v122, v118 wave_shl:1 row_mask:0xf bank_mask:0xf bound_ctrl:1
	v_add_f32_dpp v119, v123, v119 wave_shl:1 row_mask:0xf bank_mask:0xf bound_ctrl:1
	s_add_i32 s4, s34, 3
	s_cmpk_lt_i32 s4, 0x201
	s_cselect_b64 s[12:13], s[0:1], 0
	v_add_f32_dpp v118, v166, v118 wave_shr:1 row_mask:0xf bank_mask:0xf bound_ctrl:1
	v_add_f32_dpp v119, v167, v119 wave_shr:1 row_mask:0xf bank_mask:0xf bound_ctrl:1
	v_pk_fma_f32 v[118:119], v[100:101], v[146:147], v[118:119] op_sel_hi:[1,0,1] neg_lo:[0,0,1] neg_hi:[0,0,1]
	v_pk_add_f32 v[118:119], v[118:119], v[60:61] neg_lo:[0,1] neg_hi:[0,1]
	v_pk_mul_f32 v[120:121], v[118:119], v[118:119]
	v_add_f32_e32 v120, v120, v121
	v_cndmask_b32_e64 v121, 0, v120, s[12:13]
	v_add_f32_e32 v1, v1, v121
	s_waitcnt vmcnt(12)
	v_mov_b32_dpp v32, v172 wave_shr:1 row_mask:0xf bank_mask:0xf bound_ctrl:1
	v_mov_b32_dpp v33, v173 wave_shr:1 row_mask:0xf bank_mask:0xf bound_ctrl:1
	v_mov_b32_dpp v34, v174 wave_shr:1 row_mask:0xf bank_mask:0xf bound_ctrl:1
	v_mov_b32_dpp v72, v172 wave_shl:1 row_mask:0xf bank_mask:0xf bound_ctrl:1
	v_mov_b32_dpp v73, v173 wave_shl:1 row_mask:0xf bank_mask:0xf bound_ctrl:1
	v_mov_b32_dpp v74, v174 wave_shl:1 row_mask:0xf bank_mask:0xf bound_ctrl:1
	s_add_i32 s4, s34, 7
	s_cmpk_lt_u32 s4, 0x201
	s_cselect_b64 s[12:13], s[40:41], 0
	v_cmp_eq_u32_e64 s[14:15], s37, v16
	s_and_b64 s[14:15], s[14:15], s[12:13]
	v_cndmask_b32_e64 v45, 0, 1, s[14:15]
	v_pk_add_f32 v[60:61], v[172:173], v[32:33]
	v_pk_mul_f32 v[88:89], v[172:173], v[172:173] op_sel_hi:[0,1]
	v_or_b32_dpp v62, v45, v45 wave_shr:1 row_mask:0xf bank_mask:0xf bound_ctrl:1
	v_pk_mul_f32 v[94:95], v[172:173], v[174:175] op_sel_hi:[1,0]
	v_or_b32_dpp v62, v45, v62 wave_shl:1 row_mask:0xf bank_mask:0xf bound_ctrl:1
	v_mul_f32_e64 v100, v173, v173
	v_mul_f32_e64 v101, v174, v174
	v_or_b32_dpp v77, v62, v62 wave_shr:1 row_mask:0xf bank_mask:0xf bound_ctrl:1
	v_add_f32_e64 v112, v174, v34
	v_pk_add_f32 v[60:61], v[60:61], v[72:73]
	v_or_b32_dpp v77, v62, v77 wave_shl:1 row_mask:0xf bank_mask:0xf bound_ctrl:1
	v_or3_b32 v45, v77, v110, v76
	v_or3_b32 v45, v45, v63, v44
	s_add_i32 s4, s34, 4
	s_cmpk_lt_u32 s4, 0x1ff
	s_cselect_b64 s[12:13], s[42:43], 0
	v_cmp_ne_u32_e64 s[30:31], 0, v45
	s_and_b64 s[30:31], s[30:31], s[12:13]
	v_cndmask_b32_e64 v45, 0, 1.0, s[30:31]
	v_pk_fma_f32 v[88:89], v[32:33], v[32:33], v[88:89] op_sel_hi:[0,1,1]
	v_pk_fma_f32 v[94:95], v[32:33], v[34:35], v[94:95] op_sel_hi:[1,0,1]
	v_fma_f32 v100, v33, v33, v100
	v_fma_f32 v101, v34, v34, v101
	v_add_f32_dpp v113, v45, v45 wave_shr:1 row_mask:0xf bank_mask:0xf bound_ctrl:1
	v_add_f32_e64 v112, v112, v74
	v_pk_fma_f32 v[88:89], v[72:73], v[72:73], v[88:89] op_sel_hi:[0,1,1]
	v_pk_fma_f32 v[94:95], v[72:73], v[74:75], v[94:95] op_sel_hi:[1,0,1]
	v_fma_f32 v100, v73, v73, v100
	v_fma_f32 v101, v74, v74, v101
	v_add_f32_dpp v113, v45, v113 wave_shl:1 row_mask:0xf bank_mask:0xf bound_ctrl:1
	v_pk_add_f32 v[114:115], v[40:41], v[60:61]
	v_pk_add_f32 v[116:117], v[24:25], v[114:115]
	v_pk_add_f32 v[118:119], v[56:57], v[88:89]
	v_pk_add_f32 v[24:25], v[48:49], v[118:119]
	v_pk_add_f32 v[40:41], v[66:67], v[94:95]
	v_pk_add_f32 v[48:49], v[50:51], v[40:41]
	v_pk_add_f32 v[50:51], v[84:85], v[100:101]
	v_pk_add_f32 v[56:57], v[52:53], v[50:51]
	v_pk_add_f32 v[66:67], v[86:87], v[112:113]
	v_pk_add_f32 v[52:53], v[68:69], v[66:67]
	v_mul_f32_e64 v84, v116, v22
	v_mul_f32_e64 v85, v117, v22
	v_mul_f32_e64 v86, v52, v22
	v_fma_f32 v45, v24, v22, v26
	v_mul_f32_e64 v62, v25, v22
	v_mul_f32_e64 v111, v48, v22
	v_fma_f32 v68, v56, v22, v26
	v_mul_f32_e64 v69, v49, v22
	v_fma_f32 v124, v57, v22, v26
	v_fma_f32 v45, -v84, v84, v45
	v_fma_f32 v62, -v84, v85, v62
	v_fma_f32 v111, -v84, v86, v111
	v_fma_f32 v68, -v85, v85, v68
	v_fma_f32 v69, -v85, v86, v69
	v_fma_f32 v124, -v86, v86, v124
	v_mul_f32_e64 v125, v69, v69
	v_mul_f32_e64 v128, v62, v124
	v_mul_f32_e64 v129, v111, v68
	v_mul_f32_e64 v140, v111, v111
	v_mul_f32_e64 v141, v45, v69
	v_mul_f32_e64 v142, v62, v62
	v_fma_f32 v125, v68, v124, -v125
	v_fma_f32 v128, v111, v69, -v128
	v_fma_f32 v129, v62, v69, -v129
	v_fma_f32 v140, v45, v124, -v140
	v_fma_f32 v141, v62, v111, -v141
	v_fma_f32 v142, v45, v68, -v142
	v_mul_f32_e64 v143, v45, v125
	v_fma_f32 v143, v62, v128, v143
	v_fma_f32 v143, v111, v129, v143
	v_rcp_f32_e32 v143, v143
	v_cmp_ne_u32_e64 vcc, s37, v29
	v_mul_f32_e64 v143, v143, v22
	v_cndmask_b32_e64 v143, 0, v143, s[30:31]
	v_cndmask_b32_e64 v45, 0, v18, vcc
	v_cndmask_b32_e64 v133, 0, v22, s[30:31]
	v_mul_f32_e64 v87, v125, v143
	v_mul_f32_e64 v120, v128, v143
	v_mul_f32_e64 v121, v129, v143
	v_mul_f32_e64 v122, v140, v143
	v_mul_f32_e64 v123, v141, v143
	v_mul_f32_e64 v132, v142, v143
	v_add_f32_e64 v134, v53, v45
	v_mov_b32_e32 v135, v29
	ds_write_b128 v23, v[84:87]
	ds_write_b128 v23, v[120:123] offset:1024
	ds_write_b128 v23, v[132:135] offset:2048
	v_mov_b32_dpp v142, v4 wave_shr:1 row_mask:0xf bank_mask:0xf bound_ctrl:1
	v_mov_b32_dpp v143, v5 wave_shr:1 row_mask:0xf bank_mask:0xf bound_ctrl:1
	v_mov_b32_dpp v146, v4 wave_shl:1 row_mask:0xf bank_mask:0xf bound_ctrl:1
	v_mov_b32_dpp v147, v5 wave_shl:1 row_mask:0xf bank_mask:0xf bound_ctrl:1
	v_pk_mul_f32 v[24:25], v[4:5], v[172:173] op_sel_hi:[1,0]
	v_pk_mul_f32 v[44:45], v[4:5], v[172:173] op_sel:[0,1]
	v_pk_mul_f32 v[48:49], v[4:5], v[174:175] op_sel_hi:[1,0]
	v_pk_add_f32 v[52:53], v[4:5], v[142:143]
	v_pk_fma_f32 v[24:25], v[142:143], v[32:33], v[24:25] op_sel_hi:[1,0,1]
	v_pk_fma_f32 v[44:45], v[142:143], v[32:33], v[44:45] op_sel:[0,1,0]
	v_pk_fma_f32 v[48:49], v[142:143], v[34:35], v[48:49] op_sel_hi:[1,0,1]
	v_pk_add_f32 v[52:53], v[52:53], v[146:147]
	v_pk_fma_f32 v[24:25], v[146:147], v[72:73], v[24:25] op_sel_hi:[1,0,1]
	v_pk_fma_f32 v[44:45], v[146:147], v[72:73], v[44:45] op_sel:[0,1,0]
	v_pk_fma_f32 v[48:49], v[146:147], v[74:75], v[48:49] op_sel_hi:[1,0,1]
	s_waitcnt lgkmcnt(0)
	s_barrier
	s_add_i32 s5, s34, 10
	s_min_i32 s5, s5, 0x200
	s_mul_i32 s6, s5, 0x804
	s_add_i32 s6, s6, s35
	s_add_i32 s7, s6, 0x505014
	s_add_i32 s8, s6, 0x606018
	s_mul_i32 s9, s5, 0x180c
	s_add_i32 s9, s9, s33
	s_add_i32 s4, s34, 11
	s_min_i32 s4, s4, 0x200
	s_mul_i32 s4, s4, 0x804
	s_add_i32 s4, s4, s38
	buffer_load_dword v29, v28, s[20:23], s4 offen nt
	buffer_load_dwordx3 v[140:142], v27, s[24:27], s9 offen nt
	buffer_load_dword v56, v28, s[16:19], s7 offen nt
	buffer_load_dword v57, v28, s[16:19], s8 offen nt
	v_pk_add_f32 v[68:69], v[150:151], v[52:53]
	v_pk_add_f32 v[116:117], v[90:91], v[68:69]
	v_pk_add_f32 v[124:125], v[58:59], v[24:25]
	v_pk_add_f32 v[90:91], v[6:7], v[124:125]
	v_pk_add_f32 v[128:129], v[126:127], v[44:45]
	v_pk_add_f32 v[6:7], v[30:31], v[128:129]
	v_pk_add_f32 v[144:145], v[130:131], v[48:49]
	v_pk_add_f32 v[30:31], v[78:79], v[144:145]
	v_pk_fma_f32 v[90:91], v[84:85], v[116:117], v[90:91] op_sel_hi:[0,1,1] neg_lo:[1,0,0] neg_hi:[1,0,0]
	v_pk_fma_f32 v[6:7], v[84:85], v[116:117], v[6:7] op_sel:[1,0,0] neg_lo:[1,0,0] neg_hi:[1,0,0]
	v_pk_fma_f32 v[30:31], v[86:87], v[116:117], v[30:31] op_sel_hi:[0,1,1] neg_lo:[1,0,0] neg_hi:[1,0,0]
	v_pk_mul_f32 v[148:149], v[86:87], v[90:91] op_sel:[1,0]
	v_pk_mul_f32 v[164:165], v[120:121], v[90:91] op_sel_hi:[0,1]
	v_pk_mul_f32 v[176:177], v[120:121], v[90:91] op_sel:[1,0]
	v_pk_fma_f32 v[148:149], v[120:121], v[6:7], v[148:149] op_sel_hi:[0,1,1]
	v_pk_fma_f32 v[164:165], v[122:123], v[6:7], v[164:165] op_sel_hi:[0,1,1]
	v_pk_fma_f32 v[176:177], v[122:123], v[6:7], v[176:177] op_sel:[1,0,0]
	v_pk_fma_f32 v[148:149], v[120:121], v[30:31], v[148:149] op_sel:[1,0,0]
	v_pk_fma_f32 v[164:165], v[122:123], v[30:31], v[164:165] op_sel:[1,0,0]
	v_pk_fma_f32 v[176:177], v[132:133], v[30:31], v[176:177] op_sel_hi:[0,1,1]
	v_pk_mul_f32 v[58:59], v[84:85], v[148:149] op_sel_hi:[0,1]
	v_pk_fma_f32 v[58:59], v[84:85], v[164:165], v[58:59] op_sel:[1,0,0]
	v_pk_fma_f32 v[58:59], v[86:87], v[176:177], v[58:59] op_sel_hi:[0,1,1]
	v_pk_fma_f32 v[58:59], v[132:133], v[116:117], v[58:59] op_sel:[1,0,0] neg_lo:[0,0,1] neg_hi:[0,0,1]
	v_cmp_eq_u32_e64 s[10:11], 6, v135
	v_cmp_eq_u32_e64 s[14:15], 7, v135
	v_pk_add_f32 v[116:117], v[92:93], v[148:149]
	v_pk_add_f32 v[6:7], v[54:55], v[116:117]
	v_pk_add_f32 v[92:93], v[96:97], v[164:165]
	v_pk_add_f32 v[30:31], v[98:99], v[92:93]
	v_pk_add_f32 v[96:97], v[104:105], v[176:177]
	v_pk_add_f32 v[54:55], v[106:107], v[96:97]
	v_pk_add_f32 v[78:79], v[186:187], v[58:59]
	v_pk_add_f32 v[104:105], v[108:109], v[78:79]
	v_pk_fma_f32 v[108:109], v[8:9], v[6:7], v[104:105] op_sel_hi:[0,1,1]
	v_pk_fma_f32 v[180:181], v[36:37], v[6:7], v[104:105] op_sel_hi:[0,1,1]
	v_pk_fma_f32 v[108:109], v[8:9], v[30:31], v[108:109] op_sel:[1,0,0]
	v_pk_fma_f32 v[180:181], v[36:37], v[30:31], v[180:181] op_sel:[1,0,0]
	v_pk_fma_f32 v[108:109], v[10:11], v[54:55], v[108:109] op_sel_hi:[0,1,1]
	v_pk_fma_f32 v[180:181], v[38:39], v[54:55], v[180:181] op_sel_hi:[0,1,1]
	v_pk_fma_f32 v[104:105], v[152:153], v[6:7], v[104:105] op_sel_hi:[0,1,1]
	v_pk_fma_f32 v[104:105], v[152:153], v[30:31], v[104:105] op_sel:[1,0,0]
	v_pk_fma_f32 v[104:105], v[154:155], v[54:55], v[104:105] op_sel_hi:[0,1,1]
	v_cndmask_b32_e64 v90, 0, v18, s[10:11]
	v_cndmask_b32_e64 v91, 0, v18, s[14:15]
	v_add_f32_dpp v104, v108, v104 wave_shl:1 row_mask:0xf bank_mask:0xf bound_ctrl:1
	v_add_f32_dpp v105, v109, v105 wave_shl:1 row_mask:0xf bank_mask:0xf bound_ctrl:1
	s_add_i32 s4, s34, 4
	s_cmpk_lt_i32 s4, 0x201
	s_cselect_b64 s[12:13], s[0:1], 0
	v_add_f32_dpp v104, v180, v104 wave_shr:1 row_mask:0xf bank_mask:0xf bound_ctrl:1
	v_add_f32_dpp v105, v181, v105 wave_shr:1 row_mask:0xf bank_mask:0xf bound_ctrl:1
	v_pk_fma_f32 v[104:105], v[70:71], v[134:135], v[104:105] op_sel_hi:[1,0,1] neg_lo:[0,0,1] neg_hi:[0,0,1]
	v_pk_add_f32 v[104:105], v[104:105], v[90:91] neg_lo:[0,1] neg_hi:[0,1]
	v_pk_mul_f32 v[98:99], v[104:105], v[104:105]
	v_add_f32_e32 v98, v98, v99
	v_cndmask_b32_e64 v99, 0, v98, s[12:13]
	v_add_f32_e32 v1, v1, v99
	s_waitcnt vmcnt(12)
	v_mov_b32_dpp v8, v136 wave_shr:1 row_mask:0xf bank_mask:0xf bound_ctrl:1
	v_mov_b32_dpp v9, v137 wave_shr:1 row_mask:0xf bank_mask:0xf bound_ctrl:1
	v_mov_b32_dpp v10, v138 wave_shr:1 row_mask:0xf bank_mask:0xf bound_ctrl:1
	v_mov_b32_dpp v36, v136 wave_shl:1 row_mask:0xf bank_mask:0xf bound_ctrl:1
	v_mov_b32_dpp v37, v137 wave_shl:1 row_mask:0xf bank_mask:0xf bound_ctrl:1
	v_mov_b32_dpp v38, v138 wave_shl:1 row_mask:0xf bank_mask:0xf bound_ctrl:1
	s_add_i32 s4, s34, 8
	s_cmpk_lt_u32 s4, 0x201
	s_cselect_b64 s[12:13], s[40:41], 0
	v_cmp_eq_u32_e64 s[14:15], s37, v17
	s_and_b64 s[14:15], s[14:15], s[12:13]
	v_cndmask_b32_e64 v62, 0, 1, s[14:15]
	v_pk_add_f32 v[6:7], v[136:137], v[8:9]
	v_pk_mul_f32 v[30:31], v[136:137], v[136:137] op_sel_hi:[0,1]
	v_or_b32_dpp v111, v62, v62 wave_shr:1 row_mask:0xf bank_mask:0xf bound_ctrl:1
	v_pk_mul_f32 v[54:55], v[136:137], v[138:139] op_sel_hi:[1,0]
	v_or_b32_dpp v111, v62, v111 wave_shl:1 row_mask:0xf bank_mask:0xf bound_ctrl:1
	v_mul_f32_e64 v70, v137, v137
	v_mul_f32_e64 v71, v138, v138
	v_or_b32_dpp v86, v111, v111 wave_shr:1 row_mask:0xf bank_mask:0xf bound_ctrl:1
	v_add_f32_e64 v84, v138, v10
	v_pk_add_f32 v[6:7], v[6:7], v[36:37]
	v_or_b32_dpp v86, v111, v86 wave_shl:1 row_mask:0xf bank_mask:0xf bound_ctrl:1
	v_or3_b32 v62, v86, v77, v110
	v_or3_b32 v62, v62, v76, v63
	s_add_i32 s4, s34, 5
	s_cmpk_lt_u32 s4, 0x1ff
	s_cselect_b64 s[12:13], s[42:43], 0
	v_cmp_ne_u32_e64 s[30:31], 0, v62
	s_and_b64 s[30:31], s[30:31], s[12:13]
	v_cndmask_b32_e64 v62, 0, 1.0, s[30:31]
	v_pk_fma_f32 v[30:31], v[8:9], v[8:9], v[30:31] op_sel_hi:[0,1,1]
	v_pk_fma_f32 v[54:55], v[8:9], v[10:11], v[54:55] op_sel_hi:[1,0,1]
	v_fma_f32 v70, v9, v9, v70
	v_fma_f32 v71, v10, v10, v71
	v_add_f32_dpp v85, v62, v62 wave_shr:1 row_mask:0xf bank_mask:0xf bound_ctrl:1
	v_add_f32_e64 v84, v84, v38
	v_pk_fma_f32 v[30:31], v[36:37], v[36:37], v[30:31] op_sel_hi:[0,1,1]
	v_pk_fma_f32 v[54:55], v[36:37], v[38:39], v[54:55] op_sel_hi:[1,0,1]
	v_fma_f32 v70, v37, v37, v70
	v_fma_f32 v71, v38, v38, v71
	v_add_f32_dpp v85, v62, v85 wave_shl:1 row_mask:0xf bank_mask:0xf bound_ctrl:1
	v_pk_add_f32 v[90:91], v[114:115], v[6:7]
	v_pk_add_f32 v[98:99], v[118:119], v[30:31]
	v_pk_add_f32 v[104:105], v[40:41], v[54:55]
	v_pk_add_f32 v[40:41], v[50:51], v[70:71]
	v_pk_add_f32 v[50:51], v[66:67], v[84:85]
	v_mul_f32_e64 v120, v90, v22
	v_mul_f32_e64 v121, v91, v22
	v_mul_f32_e64 v122, v50, v22
	v_fma_f32 v62, v98, v22, v26
	v_mul_f32_e64 v87, v99, v22
	v_mul_f32_e64 v111, v104, v22
	v_fma_f32 v66, v40, v22, v26
	v_mul_f32_e64 v67, v105, v22
	v_fma_f32 v106, v41, v22, v26
	v_fma_f32 v62, -v120, v120, v62
	v_fma_f32 v87, -v120, v121, v87
	v_fma_f32 v111, -v120, v122, v111
	v_fma_f32 v66, -v121, v121, v66
	v_fma_f32 v67, -v121, v122, v67
	v_fma_f32 v106, -v122, v122, v106
	v_mul_f32_e64 v107, v67, v67
	v_mul_f32_e64 v108, v87, v106
	v_mul_f32_e64 v109, v111, v66
	v_mul_f32_e64 v114, v111, v111
	v_mul_f32_e64 v115, v62, v67
	v_mul_f32_e64 v118, v87, v87
	v_fma_f32 v107, v66, v106, -v107
	v_fma_f32 v108, v111, v67, -v108
	v_fma_f32 v109, v87, v67, -v109
	v_fma_f32 v114, v62, v106, -v114
	v_fma_f32 v115, v87, v111, -v115
	v_fma_f32 v118, v62, v66, -v118
	v_mul_f32_e64 v119, v62, v107
	v_fma_f32 v119, v87, v108, v119
	v_fma_f32 v119, v111, v109, v119
	v_rcp_f32_e32 v119, v119
	v_cmp_ne_u32_e64 vcc, s37, v2
	v_mul_f32_e64 v119, v119, v22
	v_cndmask_b32_e64 v119, 0, v119, s[30:31]
	v_cndmask_b32_e64 v62, 0, v18, vcc
	v_cndmask_b32_e64 v153, 0, v22, s[30:31]
	v_mul_f32_e64 v123, v107, v119
	v_mul_f32_e64 v132, v108, v119
	v_mul_f32_e64 v133, v109, v119
	v_mul_f32_e64 v134, v114, v119
	v_mul_f32_e64 v135, v115, v119
	v_mul_f32_e64 v152, v118, v119
	v_add_f32_e64 v154, v51, v62
	v_mov_b32_e32 v155, v2
	ds_write_b128 v23, v[120:123] offset:3072
	ds_write_b128 v23, v[132:135] offset:4096
	ds_write_b128 v23, v[152:155] offset:5120
	v_mov_b32_dpp v40, v102 wave_shr:1 row_mask:0xf bank_mask:0xf bound_ctrl:1
	v_mov_b32_dpp v41, v103 wave_shr:1 row_mask:0xf bank_mask:0xf bound_ctrl:1
	v_mov_b32_dpp v104, v102 wave_shl:1 row_mask:0xf bank_mask:0xf bound_ctrl:1
	v_mov_b32_dpp v105, v103 wave_shl:1 row_mask:0xf bank_mask:0xf bound_ctrl:1
	v_pk_mul_f32 v[50:51], v[102:103], v[136:137] op_sel_hi:[1,0]
	v_pk_mul_f32 v[62:63], v[102:103], v[136:137] op_sel:[0,1]
	v_pk_mul_f32 v[66:67], v[102:103], v[138:139] op_sel_hi:[1,0]
	v_pk_add_f32 v[90:91], v[102:103], v[40:41]
	v_pk_fma_f32 v[50:51], v[40:41], v[8:9], v[50:51] op_sel_hi:[1,0,1]
	v_pk_fma_f32 v[62:63], v[40:41], v[8:9], v[62:63] op_sel:[0,1,0]
	v_pk_fma_f32 v[66:67], v[40:41], v[10:11], v[66:67] op_sel_hi:[1,0,1]
	v_pk_add_f32 v[90:91], v[90:91], v[104:105]
	v_pk_fma_f32 v[50:51], v[104:105], v[36:37], v[50:51] op_sel_hi:[1,0,1]
	v_pk_fma_f32 v[62:63], v[104:105], v[36:37], v[62:63] op_sel:[0,1,0]
	v_pk_fma_f32 v[66:67], v[104:105], v[38:39], v[66:67] op_sel_hi:[1,0,1]
	s_waitcnt lgkmcnt(0)
	s_barrier
	s_add_i32 s5, s34, 11
	s_min_i32 s5, s5, 0x200
	s_mul_i32 s6, s5, 0x804
	s_add_i32 s6, s6, s35
	s_add_i32 s7, s6, 0x505014
	s_add_i32 s8, s6, 0x606018
	s_mul_i32 s9, s5, 0x180c
	s_add_i32 s9, s9, s33
	s_add_i32 s4, s34, 12
	s_min_i32 s4, s4, 0x200
	s_mul_i32 s4, s4, 0x804
	s_add_i32 s4, s4, s38
	buffer_load_dword v2, v28, s[20:23], s4 offen nt
	buffer_load_dwordx3 v[104:106], v27, s[24:27], s9 offen nt
	buffer_load_dword v40, v28, s[16:19], s7 offen nt
	buffer_load_dword v41, v28, s[16:19], s8 offen nt
	v_pk_add_f32 v[98:99], v[68:69], v[90:91]
	v_pk_add_f32 v[68:69], v[124:125], v[50:51]
	v_pk_add_f32 v[108:109], v[128:129], v[62:63]
	v_pk_add_f32 v[124:125], v[144:145], v[66:67]
	v_pk_fma_f32 v[68:69], v[120:121], v[98:99], v[68:69] op_sel_hi:[0,1,1] neg_lo:[1,0,0] neg_hi:[1,0,0]
	v_pk_fma_f32 v[108:109], v[120:121], v[98:99], v[108:109] op_sel:[1,0,0] neg_lo:[1,0,0] neg_hi:[1,0,0]
	v_pk_fma_f32 v[124:125], v[122:123], v[98:99], v[124:125] op_sel_hi:[0,1,1] neg_lo:[1,0,0] neg_hi:[1,0,0]
	v_pk_mul_f32 v[114:115], v[122:123], v[68:69] op_sel:[1,0]
	v_pk_mul_f32 v[118:119], v[132:133], v[68:69] op_sel_hi:[0,1]
	v_pk_mul_f32 v[126:127], v[132:133], v[68:69] op_sel:[1,0]
	v_pk_fma_f32 v[114:115], v[132:133], v[108:109], v[114:115] op_sel_hi:[0,1,1]
	v_pk_fma_f32 v[118:119], v[134:135], v[108:109], v[118:119] op_sel_hi:[0,1,1]
	v_pk_fma_f32 v[126:127], v[134:135], v[108:109], v[126:127] op_sel:[1,0,0]
	v_pk_fma_f32 v[114:115], v[132:133], v[124:125], v[114:115] op_sel:[1,0,0]
	v_pk_fma_f32 v[118:119], v[134:135], v[124:125], v[118:119] op_sel:[1,0,0]
	v_pk_fma_f32 v[126:127], v[152:153], v[124:125], v[126:127] op_sel_hi:[0,1,1]
	v_pk_mul_f32 v[128:129], v[120:121], v[114:115] op_sel_hi:[0,1]
	v_pk_fma_f32 v[128:129], v[120:121], v[118:119], v[128:129] op_sel:[1,0,0]
	v_pk_fma_f32 v[128:129], v[122:123], v[126:127], v[128:129] op_sel_hi:[0,1,1]
	v_pk_fma_f32 v[128:129], v[152:153], v[98:99], v[128:129] op_sel:[1,0,0] neg_lo:[0,0,1] neg_hi:[0,0,1]
	v_cmp_eq_u32_e64 s[10:11], 6, v155
	v_cmp_eq_u32_e64 s[14:15], 7, v155
	v_pk_add_f32 v[68:69], v[116:117], v[114:115]
	v_pk_add_f32 v[98:99], v[92:93], v[118:119]
	v_pk_add_f32 v[92:93], v[96:97], v[126:127]
	v_pk_add_f32 v[130:131], v[78:79], v[128:129]
	v_pk_fma_f32 v[78:79], v[12:13], v[68:69], v[130:131] op_sel_hi:[0,1,1]
	v_pk_fma_f32 v[146:147], v[80:81], v[68:69], v[130:131] op_sel_hi:[0,1,1]
	v_pk_fma_f32 v[78:79], v[12:13], v[98:99], v[78:79] op_sel:[1,0,0]
	v_pk_fma_f32 v[146:147], v[80:81], v[98:99], v[146:147] op_sel:[1,0,0]
	v_pk_fma_f32 v[78:79], v[14:15], v[92:93], v[78:79] op_sel_hi:[0,1,1]
	v_pk_fma_f32 v[146:147], v[82:83], v[92:93], v[146:147] op_sel_hi:[0,1,1]
	v_pk_fma_f32 v[130:131], v[160:161], v[68:69], v[130:131] op_sel_hi:[0,1,1]
	v_pk_fma_f32 v[130:131], v[160:161], v[98:99], v[130:131] op_sel:[1,0,0]
	v_pk_fma_f32 v[130:131], v[162:163], v[92:93], v[130:131] op_sel_hi:[0,1,1]
	v_cndmask_b32_e64 v96, 0, v18, s[10:11]
	v_cndmask_b32_e64 v97, 0, v18, s[14:15]
	v_add_f32_dpp v130, v78, v130 wave_shl:1 row_mask:0xf bank_mask:0xf bound_ctrl:1
	v_add_f32_dpp v131, v79, v131 wave_shl:1 row_mask:0xf bank_mask:0xf bound_ctrl:1
	s_add_i32 s4, s34, 5
	s_cmpk_lt_i32 s4, 0x201
	s_cselect_b64 s[12:13], s[0:1], 0
	v_add_f32_dpp v130, v146, v130 wave_shr:1 row_mask:0xf bank_mask:0xf bound_ctrl:1
	v_add_f32_dpp v131, v147, v131 wave_shr:1 row_mask:0xf bank_mask:0xf bound_ctrl:1
	v_pk_fma_f32 v[130:131], v[46:47], v[154:155], v[130:131] op_sel_hi:[1,0,1] neg_lo:[0,0,1] neg_hi:[0,0,1]
	v_pk_add_f32 v[130:131], v[130:131], v[96:97] neg_lo:[0,1] neg_hi:[0,1]
	v_pk_mul_f32 v[108:109], v[130:131], v[130:131]
	v_add_f32_e32 v108, v108, v109
	v_cndmask_b32_e64 v109, 0, v108, s[12:13]
	v_add_f32_e32 v1, v1, v109
	s_waitcnt vmcnt(12)
	v_mov_b32_dpp v12, v168 wave_shr:1 row_mask:0xf bank_mask:0xf bound_ctrl:1
	v_mov_b32_dpp v13, v169 wave_shr:1 row_mask:0xf bank_mask:0xf bound_ctrl:1
	v_mov_b32_dpp v14, v170 wave_shr:1 row_mask:0xf bank_mask:0xf bound_ctrl:1
	v_mov_b32_dpp v80, v168 wave_shl:1 row_mask:0xf bank_mask:0xf bound_ctrl:1
	v_mov_b32_dpp v81, v169 wave_shl:1 row_mask:0xf bank_mask:0xf bound_ctrl:1
	v_mov_b32_dpp v82, v170 wave_shl:1 row_mask:0xf bank_mask:0xf bound_ctrl:1
	s_add_i32 s4, s34, 9
	s_cmpk_lt_u32 s4, 0x201
	s_cselect_b64 s[12:13], s[40:41], 0
	v_cmp_eq_u32_e64 s[14:15], s37, v43
	s_and_b64 s[14:15], s[14:15], s[12:13]
	v_cndmask_b32_e64 v87, 0, 1, s[14:15]
	v_pk_add_f32 v[46:47], v[168:169], v[12:13]
	v_pk_mul_f32 v[68:69], v[168:169], v[168:169] op_sel_hi:[0,1]
	v_or_b32_dpp v111, v87, v87 wave_shr:1 row_mask:0xf bank_mask:0xf bound_ctrl:1
	v_pk_mul_f32 v[78:79], v[168:169], v[170:171] op_sel_hi:[1,0]
	v_or_b32_dpp v111, v87, v111 wave_shl:1 row_mask:0xf bank_mask:0xf bound_ctrl:1
	v_mul_f32_e64 v92, v169, v169
	v_mul_f32_e64 v93, v170, v170
	v_or_b32_dpp v98, v111, v111 wave_shr:1 row_mask:0xf bank_mask:0xf bound_ctrl:1
	v_add_f32_e64 v96, v170, v14
	v_pk_add_f32 v[46:47], v[46:47], v[80:81]
	v_or_b32_dpp v98, v111, v98 wave_shl:1 row_mask:0xf bank_mask:0xf bound_ctrl:1
	v_or3_b32 v87, v98, v86, v77
	v_or3_b32 v87, v87, v110, v76
	s_add_i32 s4, s34, 6
	s_cmpk_lt_u32 s4, 0x1ff
	s_cselect_b64 s[12:13], s[42:43], 0
	v_cmp_ne_u32_e64 s[30:31], 0, v87
	s_and_b64 s[30:31], s[30:31], s[12:13]
	v_cndmask_b32_e64 v87, 0, 1.0, s[30:31]
	v_pk_fma_f32 v[68:69], v[12:13], v[12:13], v[68:69] op_sel_hi:[0,1,1]
	v_pk_fma_f32 v[78:79], v[12:13], v[14:15], v[78:79] op_sel_hi:[1,0,1]
	v_fma_f32 v92, v13, v13, v92
	v_fma_f32 v93, v14, v14, v93
	v_add_f32_dpp v97, v87, v87 wave_shr:1 row_mask:0xf bank_mask:0xf bound_ctrl:1
	v_add_f32_e64 v96, v96, v82
	v_pk_fma_f32 v[68:69], v[80:81], v[80:81], v[68:69] op_sel_hi:[0,1,1]
	v_pk_fma_f32 v[78:79], v[80:81], v[82:83], v[78:79] op_sel_hi:[1,0,1]
	v_fma_f32 v92, v81, v81, v92
	v_fma_f32 v93, v82, v82, v93
	v_add_f32_dpp v97, v87, v97 wave_shl:1 row_mask:0xf bank_mask:0xf bound_ctrl:1
	v_pk_add_f32 v[122:123], v[6:7], v[46:47]
	v_pk_add_f32 v[108:109], v[60:61], v[122:123]
	v_pk_add_f32 v[6:7], v[30:31], v[68:69]
	v_pk_add_f32 v[60:61], v[88:89], v[6:7]
	v_pk_add_f32 v[88:89], v[54:55], v[78:79]
	v_pk_add_f32 v[30:31], v[94:95], v[88:89]
	v_pk_add_f32 v[54:55], v[70:71], v[92:93]
	v_pk_add_f32 v[94:95], v[100:101], v[54:55]
	v_pk_add_f32 v[70:71], v[84:85], v[96:97]
	v_pk_add_f32 v[100:101], v[112:113], v[70:71]
	v_mul_f32_e64 v132, v108, v22
	v_mul_f32_e64 v133, v109, v22
	v_mul_f32_e64 v134, v100, v22
	v_fma_f32 v87, v60, v22, v26
	v_mul_f32_e64 v99, v61, v22
	v_mul_f32_e64 v111, v30, v22
	v_fma_f32 v84, v94, v22, v26
	v_mul_f32_e64 v85, v31, v22
	v_fma_f32 v112, v95, v22, v26
	v_fma_f32 v87, -v132, v132, v87
	v_fma_f32 v99, -v132, v133, v99
	v_fma_f32 v111, -v132, v134, v111
	v_fma_f32 v84, -v133, v133, v84
	v_fma_f32 v85, -v133, v134, v85
	v_fma_f32 v112, -v134, v134, v112
	v_mul_f32_e64 v113, v85, v85
	v_mul_f32_e64 v116, v99, v112
	v_mul_f32_e64 v117, v111, v84
	v_mul_f32_e64 v120, v111, v111
	v_mul_f32_e64 v121, v87, v85
	v_mul_f32_e64 v124, v99, v99
	v_fma_f32 v113, v84, v112, -v113
	v_fma_f32 v116, v111, v85, -v116
	v_fma_f32 v117, v99, v85, -v117
	v_fma_f32 v120, v87, v112, -v120
	v_fma_f32 v121, v99, v111, -v121
	v_fma_f32 v124, v87, v84, -v124
	v_mul_f32_e64 v125, v87, v113
	v_fma_f32 v125, v99, v116, v125
	v_fma_f32 v125, v111, v117, v125
	v_rcp_f32_e32 v125, v125
	v_cmp_ne_u32_e64 vcc, s37, v3
	v_mul_f32_e64 v125, v125, v22
	v_cndmask_b32_e64 v125, 0, v125, s[30:31]
	v_cndmask_b32_e64 v87, 0, v18, vcc
	v_cndmask_b32_e64 v153, 0, v22, s[30:31]
	v_mul_f32_e64 v135, v113, v125
	v_mul_f32_e64 v144, v116, v125
	v_mul_f32_e64 v145, v117, v125
	v_mul_f32_e64 v146, v120, v125
	v_mul_f32_e64 v147, v121, v125
	v_mul_f32_e64 v152, v124, v125
	v_add_f32_e64 v154, v101, v87
	v_mov_b32_e32 v155, v3
	ds_write_b128 v23, v[132:135]
	ds_write_b128 v23, v[144:147] offset:1024
	ds_write_b128 v23, v[152:155] offset:2048
	v_mov_b32_dpp v30, v64 wave_shr:1 row_mask:0xf bank_mask:0xf bound_ctrl:1
	v_mov_b32_dpp v31, v65 wave_shr:1 row_mask:0xf bank_mask:0xf bound_ctrl:1
	v_mov_b32_dpp v94, v64 wave_shl:1 row_mask:0xf bank_mask:0xf bound_ctrl:1
	v_mov_b32_dpp v95, v65 wave_shl:1 row_mask:0xf bank_mask:0xf bound_ctrl:1
	v_pk_mul_f32 v[60:61], v[64:65], v[168:169] op_sel_hi:[1,0]
	v_pk_mul_f32 v[84:85], v[64:65], v[168:169] op_sel:[0,1]
	v_pk_mul_f32 v[100:101], v[64:65], v[170:171] op_sel_hi:[1,0]
	v_pk_add_f32 v[108:109], v[64:65], v[30:31]
	v_pk_fma_f32 v[60:61], v[30:31], v[12:13], v[60:61] op_sel_hi:[1,0,1]
	v_pk_fma_f32 v[84:85], v[30:31], v[12:13], v[84:85] op_sel:[0,1,0]
	v_pk_fma_f32 v[100:101], v[30:31], v[14:15], v[100:101] op_sel_hi:[1,0,1]
	v_pk_add_f32 v[108:109], v[108:109], v[94:95]
	v_pk_fma_f32 v[60:61], v[94:95], v[80:81], v[60:61] op_sel_hi:[1,0,1]
	v_pk_fma_f32 v[84:85], v[94:95], v[80:81], v[84:85] op_sel:[0,1,0]
	v_pk_fma_f32 v[100:101], v[94:95], v[82:83], v[100:101] op_sel_hi:[1,0,1]
	s_waitcnt lgkmcnt(0)
	s_barrier
	v_pk_add_f32 v[30:31], v[90:91], v[108:109]
	v_pk_add_f32 v[94:95], v[52:53], v[30:31]
	v_pk_add_f32 v[90:91], v[50:51], v[60:61]
	v_pk_add_f32 v[52:53], v[24:25], v[90:91]
	v_pk_add_f32 v[50:51], v[62:63], v[84:85]
	v_pk_add_f32 v[24:25], v[44:45], v[50:51]
	v_pk_add_f32 v[62:63], v[66:67], v[100:101]
	v_pk_add_f32 v[44:45], v[48:49], v[62:63]
	v_pk_fma_f32 v[52:53], v[132:133], v[94:95], v[52:53] op_sel_hi:[0,1,1] neg_lo:[1,0,0] neg_hi:[1,0,0]
	v_pk_fma_f32 v[24:25], v[132:133], v[94:95], v[24:25] op_sel:[1,0,0] neg_lo:[1,0,0] neg_hi:[1,0,0]
	v_pk_fma_f32 v[44:45], v[134:135], v[94:95], v[44:45] op_sel_hi:[0,1,1] neg_lo:[1,0,0] neg_hi:[1,0,0]
	v_pk_mul_f32 v[66:67], v[134:135], v[52:53] op_sel:[1,0]
	v_pk_mul_f32 v[130:131], v[144:145], v[52:53] op_sel_hi:[0,1]
	v_pk_mul_f32 v[150:151], v[144:145], v[52:53] op_sel:[1,0]
	v_pk_fma_f32 v[66:67], v[144:145], v[24:25], v[66:67] op_sel_hi:[0,1,1]
	v_pk_fma_f32 v[130:131], v[146:147], v[24:25], v[130:131] op_sel_hi:[0,1,1]
	v_pk_fma_f32 v[150:151], v[146:147], v[24:25], v[150:151] op_sel:[1,0,0]
	v_pk_fma_f32 v[66:67], v[144:145], v[44:45], v[66:67] op_sel:[1,0,0]
	v_pk_fma_f32 v[130:131], v[146:147], v[44:45], v[130:131] op_sel:[1,0,0]
	v_pk_fma_f32 v[150:151], v[152:153], v[44:45], v[150:151] op_sel_hi:[0,1,1]
	v_pk_mul_f32 v[48:49], v[132:133], v[66:67] op_sel_hi:[0,1]
	v_pk_fma_f32 v[48:49], v[132:133], v[130:131], v[48:49] op_sel:[1,0,0]
	v_pk_fma_f32 v[48:49], v[134:135], v[150:151], v[48:49] op_sel_hi:[0,1,1]
	v_pk_fma_f32 v[48:49], v[152:153], v[94:95], v[48:49] op_sel:[1,0,0] neg_lo:[0,0,1] neg_hi:[0,0,1]
	v_cmp_eq_u32_e64 s[10:11], 6, v155
	v_cmp_eq_u32_e64 s[14:15], 7, v155
	v_pk_add_f32 v[94:95], v[114:115], v[66:67]
	v_pk_add_f32 v[24:25], v[148:149], v[94:95]
	v_pk_add_f32 v[114:115], v[118:119], v[130:131]
	v_pk_add_f32 v[44:45], v[164:165], v[114:115]
	v_pk_add_f32 v[118:119], v[126:127], v[150:151]
	v_pk_add_f32 v[52:53], v[176:177], v[118:119]
	v_pk_add_f32 v[112:113], v[128:129], v[48:49]
	v_pk_add_f32 v[126:127], v[58:59], v[112:113]
	v_pk_fma_f32 v[58:59], v[32:33], v[24:25], v[126:127] op_sel_hi:[0,1,1]
	v_pk_fma_f32 v[162:163], v[72:73], v[24:25], v[126:127] op_sel_hi:[0,1,1]
	v_pk_fma_f32 v[58:59], v[32:33], v[44:45], v[58:59] op_sel:[1,0,0]
	v_pk_fma_f32 v[162:163], v[72:73], v[44:45], v[162:163] op_sel:[1,0,0]
	v_pk_fma_f32 v[58:59], v[34:35], v[52:53], v[58:59] op_sel_hi:[0,1,1]
	v_pk_fma_f32 v[162:163], v[74:75], v[52:53], v[162:163] op_sel_hi:[0,1,1]
	v_pk_fma_f32 v[126:127], v[172:173], v[24:25], v[126:127] op_sel_hi:[0,1,1]
	v_pk_fma_f32 v[126:127], v[172:173], v[44:45], v[126:127] op_sel:[1,0,0]
	v_pk_fma_f32 v[126:127], v[174:175], v[52:53], v[126:127] op_sel_hi:[0,1,1]
	v_cndmask_b32_e64 v116, 0, v18, s[10:11]
	v_cndmask_b32_e64 v117, 0, v18, s[14:15]
	v_add_f32_dpp v126, v58, v126 wave_shl:1 row_mask:0xf bank_mask:0xf bound_ctrl:1
	v_add_f32_dpp v127, v59, v127 wave_shl:1 row_mask:0xf bank_mask:0xf bound_ctrl:1
	s_add_i32 s4, s34, 6
	s_cmpk_lt_i32 s4, 0x201
	s_cselect_b64 s[12:13], s[0:1], 0
	v_add_f32_dpp v126, v162, v126 wave_shr:1 row_mask:0xf bank_mask:0xf bound_ctrl:1
	v_add_f32_dpp v127, v163, v127 wave_shr:1 row_mask:0xf bank_mask:0xf bound_ctrl:1
	v_pk_fma_f32 v[126:127], v[4:5], v[154:155], v[126:127] op_sel_hi:[1,0,1] neg_lo:[0,0,1] neg_hi:[0,0,1]
	v_pk_add_f32 v[126:127], v[126:127], v[116:117] neg_lo:[0,1] neg_hi:[0,1]
	v_pk_mul_f32 v[120:121], v[126:127], v[126:127]
	v_add_f32_e32 v120, v120, v121
	v_cndmask_b32_e64 v121, 0, v120, s[12:13]
	v_add_f32_e32 v1, v1, v121
	s_waitcnt vmcnt(8)
	v_mov_b32_dpp v32, v156 wave_shr:1 row_mask:0xf bank_mask:0xf bound_ctrl:1
	v_mov_b32_dpp v33, v157 wave_shr:1 row_mask:0xf bank_mask:0xf bound_ctrl:1
	v_mov_b32_dpp v34, v158 wave_shr:1 row_mask:0xf bank_mask:0xf bound_ctrl:1
	v_mov_b32_dpp v72, v156 wave_shl:1 row_mask:0xf bank_mask:0xf bound_ctrl:1
	v_mov_b32_dpp v73, v157 wave_shl:1 row_mask:0xf bank_mask:0xf bound_ctrl:1
	v_mov_b32_dpp v74, v158 wave_shl:1 row_mask:0xf bank_mask:0xf bound_ctrl:1
	s_add_i32 s4, s34, 10
	s_cmpk_lt_u32 s4, 0x201
	s_cselect_b64 s[12:13], s[40:41], 0
	v_cmp_eq_u32_e64 s[14:15], s37, v42
	s_and_b64 s[14:15], s[14:15], s[12:13]
	v_cndmask_b32_e64 v3, 0, 1, s[14:15]
	v_pk_add_f32 v[4:5], v[156:157], v[32:33]
	v_pk_mul_f32 v[24:25], v[156:157], v[156:157] op_sel_hi:[0,1]
	v_or_b32_dpp v76, v3, v3 wave_shr:1 row_mask:0xf bank_mask:0xf bound_ctrl:1
	v_pk_mul_f32 v[44:45], v[156:157], v[158:159] op_sel_hi:[1,0]
	v_or_b32_dpp v76, v3, v76 wave_shl:1 row_mask:0xf bank_mask:0xf bound_ctrl:1
	v_mul_f32_e64 v52, v157, v157
	v_mul_f32_e64 v53, v158, v158
	v_or_b32_dpp v87, v76, v76 wave_shr:1 row_mask:0xf bank_mask:0xf bound_ctrl:1
	v_add_f32_e64 v58, v158, v34
	v_pk_add_f32 v[4:5], v[4:5], v[72:73]
	v_or_b32_dpp v87, v76, v87 wave_shl:1 row_mask:0xf bank_mask:0xf bound_ctrl:1
	v_or3_b32 v3, v87, v98, v86
	v_or3_b32 v3, v3, v77, v110
	s_add_i32 s4, s34, 7
	s_cmpk_lt_u32 s4, 0x1ff
	s_cselect_b64 s[12:13], s[42:43], 0
	v_cmp_ne_u32_e64 s[30:31], 0, v3
	s_and_b64 s[30:31], s[30:31], s[12:13]
	v_cndmask_b32_e64 v3, 0, 1.0, s[30:31]
	v_pk_fma_f32 v[24:25], v[32:33], v[32:33], v[24:25] op_sel_hi:[0,1,1]
	v_pk_fma_f32 v[44:45], v[32:33], v[34:35], v[44:45] op_sel_hi:[1,0,1]
	v_fma_f32 v52, v33, v33, v52
	v_fma_f32 v53, v34, v34, v53
	v_add_f32_dpp v59, v3, v3 wave_shr:1 row_mask:0xf bank_mask:0xf bound_ctrl:1
	v_add_f32_e64 v58, v58, v74
	v_pk_fma_f32 v[24:25], v[72:73], v[72:73], v[24:25] op_sel_hi:[0,1,1]
	v_pk_fma_f32 v[44:45], v[72:73], v[74:75], v[44:45] op_sel_hi:[1,0,1]
	v_fma_f32 v52, v73, v73, v52
	v_fma_f32 v53, v74, v74, v53
	v_add_f32_dpp v59, v3, v59 wave_shl:1 row_mask:0xf bank_mask:0xf bound_ctrl:1
	v_pk_add_f32 v[116:117], v[122:123], v[4:5]
	v_pk_add_f32 v[120:121], v[6:7], v[24:25]
	v_pk_add_f32 v[6:7], v[88:89], v[44:45]
	v_pk_add_f32 v[88:89], v[54:55], v[52:53]
	v_pk_add_f32 v[54:55], v[70:71], v[58:59]
	v_mul_f32_e64 v124, v116, v22
	v_mul_f32_e64 v125, v117, v22
	v_mul_f32_e64 v126, v54, v22
	v_fma_f32 v3, v120, v22, v26
	v_mul_f32_e64 v76, v121, v22
	v_mul_f32_e64 v99, v6, v22
	v_fma_f32 v111, v88, v22, v26
	v_mul_f32_e64 v70, v7, v22
	v_fma_f32 v71, v89, v22, v26
	v_fma_f32 v3, -v124, v124, v3
	v_fma_f32 v76, -v124, v125, v76
	v_fma_f32 v99, -v124, v126, v99
	v_fma_f32 v111, -v125, v125, v111
	v_fma_f32 v70, -v125, v126, v70
	v_fma_f32 v71, -v126, v126, v71
	v_mul_f32_e64 v122, v70, v70
	v_mul_f32_e64 v123, v76, v71
	v_mul_f32_e64 v128, v99, v111
	v_mul_f32_e64 v129, v99, v99
	v_mul_f32_e64 v148, v3, v70
	v_mul_f32_e64 v149, v76, v76
	v_fma_f32 v122, v111, v71, -v122
	v_fma_f32 v123, v99, v70, -v123
	v_fma_f32 v128, v76, v70, -v128
	v_fma_f32 v129, v3, v71, -v129
	v_fma_f32 v148, v76, v99, -v148
	v_fma_f32 v149, v3, v111, -v149
	v_mul_f32_e64 v152, v3, v122
	v_fma_f32 v152, v76, v123, v152
	v_fma_f32 v152, v99, v128, v152
	v_rcp_f32_e32 v152, v152
	v_cmp_ne_u32_e64 vcc, s37, v16
	v_mul_f32_e64 v152, v152, v22
	v_cndmask_b32_e64 v152, 0, v152, s[30:31]
	v_cndmask_b32_e64 v3, 0, v18, vcc
	v_cndmask_b32_e64 v145, 0, v22, s[30:31]
	v_mul_f32_e64 v127, v122, v152
	v_mul_f32_e64 v132, v123, v152
	v_mul_f32_e64 v133, v128, v152
	v_mul_f32_e64 v134, v129, v152
	v_mul_f32_e64 v135, v148, v152
	v_mul_f32_e64 v144, v149, v152
	v_add_f32_e64 v146, v55, v3
	v_mov_b32_e32 v147, v16
	ds_write_b128 v23, v[124:127] offset:3072
	ds_write_b128 v23, v[132:135] offset:4096
	ds_write_b128 v23, v[144:147] offset:5120
	v_mov_b32_dpp v6, v20 wave_shr:1 row_mask:0xf bank_mask:0xf bound_ctrl:1
	v_mov_b32_dpp v7, v21 wave_shr:1 row_mask:0xf bank_mask:0xf bound_ctrl:1
	v_mov_b32_dpp v54, v20 wave_shl:1 row_mask:0xf bank_mask:0xf bound_ctrl:1
	v_mov_b32_dpp v55, v21 wave_shl:1 row_mask:0xf bank_mask:0xf bound_ctrl:1
	v_pk_mul_f32 v[88:89], v[20:21], v[156:157] op_sel_hi:[1,0]
	v_pk_mul_f32 v[116:117], v[20:21], v[156:157] op_sel:[0,1]
	v_pk_mul_f32 v[120:121], v[20:21], v[158:159] op_sel_hi:[1,0]
	v_pk_add_f32 v[128:129], v[20:21], v[6:7]
	v_pk_fma_f32 v[88:89], v[6:7], v[32:33], v[88:89] op_sel_hi:[1,0,1]
	v_pk_fma_f32 v[116:117], v[6:7], v[32:33], v[116:117] op_sel:[0,1,0]
	v_pk_fma_f32 v[120:121], v[6:7], v[34:35], v[120:121] op_sel_hi:[1,0,1]
	v_pk_add_f32 v[128:129], v[128:129], v[54:55]
	v_pk_fma_f32 v[88:89], v[54:55], v[72:73], v[88:89] op_sel_hi:[1,0,1]
	v_pk_fma_f32 v[116:117], v[54:55], v[72:73], v[116:117] op_sel:[0,1,0]
	v_pk_fma_f32 v[120:121], v[54:55], v[74:75], v[120:121] op_sel_hi:[1,0,1]
	s_waitcnt lgkmcnt(0)
	s_barrier
	v_pk_add_f32 v[6:7], v[30:31], v[128:129]
	v_pk_add_f32 v[148:149], v[90:91], v[88:89]
	v_pk_add_f32 v[152:153], v[50:51], v[116:117]
	v_pk_add_f32 v[160:161], v[62:63], v[120:121]
	v_pk_fma_f32 v[148:149], v[124:125], v[6:7], v[148:149] op_sel_hi:[0,1,1] neg_lo:[1,0,0] neg_hi:[1,0,0]
	v_pk_fma_f32 v[152:153], v[124:125], v[6:7], v[152:153] op_sel:[1,0,0] neg_lo:[1,0,0] neg_hi:[1,0,0]
	v_pk_fma_f32 v[160:161], v[126:127], v[6:7], v[160:161] op_sel_hi:[0,1,1] neg_lo:[1,0,0] neg_hi:[1,0,0]
	v_pk_mul_f32 v[30:31], v[126:127], v[148:149] op_sel:[1,0]
	v_pk_mul_f32 v[50:51], v[132:133], v[148:149] op_sel_hi:[0,1]
	v_pk_mul_f32 v[54:55], v[132:133], v[148:149] op_sel:[1,0]
	v_pk_fma_f32 v[30:31], v[132:133], v[152:153], v[30:31] op_sel_hi:[0,1,1]
	v_pk_fma_f32 v[50:51], v[134:135], v[152:153], v[50:51] op_sel_hi:[0,1,1]
	v_pk_fma_f32 v[54:55], v[134:135], v[152:153], v[54:55] op_sel:[1,0,0]
	v_pk_fma_f32 v[30:31], v[132:133], v[160:161], v[30:31] op_sel:[1,0,0]
	v_pk_fma_f32 v[50:51], v[134:135], v[160:161], v[50:51] op_sel:[1,0,0]
	v_pk_fma_f32 v[54:55], v[144:145], v[160:161], v[54:55] op_sel_hi:[0,1,1]
	v_pk_mul_f32 v[164:165], v[124:125], v[30:31] op_sel_hi:[0,1]
	v_pk_fma_f32 v[164:165], v[124:125], v[50:51], v[164:165] op_sel:[1,0,0]
	v_pk_fma_f32 v[164:165], v[126:127], v[54:55], v[164:165] op_sel_hi:[0,1,1]
	v_pk_fma_f32 v[164:165], v[144:145], v[6:7], v[164:165] op_sel:[1,0,0] neg_lo:[0,0,1] neg_hi:[0,0,1]
	v_cmp_eq_u32_e64 s[10:11], 6, v147
	v_cmp_eq_u32_e64 s[14:15], 7, v147
	v_pk_add_f32 v[6:7], v[94:95], v[30:31]
	v_pk_add_f32 v[62:63], v[114:115], v[50:51]
	v_pk_add_f32 v[70:71], v[118:119], v[54:55]
	v_pk_add_f32 v[148:149], v[112:113], v[164:165]
	v_pk_fma_f32 v[112:113], v[8:9], v[6:7], v[148:149] op_sel_hi:[0,1,1]
	v_pk_fma_f32 v[152:153], v[36:37], v[6:7], v[148:149] op_sel_hi:[0,1,1]
	v_pk_fma_f32 v[112:113], v[8:9], v[62:63], v[112:113] op_sel:[1,0,0]
	v_pk_fma_f32 v[152:153], v[36:37], v[62:63], v[152:153] op_sel:[1,0,0]
	v_pk_fma_f32 v[112:113], v[10:11], v[70:71], v[112:113] op_sel_hi:[0,1,1]
	v_pk_fma_f32 v[152:153], v[38:39], v[70:71], v[152:153] op_sel_hi:[0,1,1]
	v_pk_fma_f32 v[148:149], v[136:137], v[6:7], v[148:149] op_sel_hi:[0,1,1]
	v_pk_fma_f32 v[148:149], v[136:137], v[62:63], v[148:149] op_sel:[1,0,0]
	v_pk_fma_f32 v[148:149], v[138:139], v[70:71], v[148:149] op_sel_hi:[0,1,1]
	v_cndmask_b32_e64 v90, 0, v18, s[10:11]
	v_cndmask_b32_e64 v91, 0, v18, s[14:15]
	v_add_f32_dpp v148, v112, v148 wave_shl:1 row_mask:0xf bank_mask:0xf bound_ctrl:1
	v_add_f32_dpp v149, v113, v149 wave_shl:1 row_mask:0xf bank_mask:0xf bound_ctrl:1
	s_add_i32 s4, s34, 7
	s_cmpk_lt_i32 s4, 0x201
	s_cselect_b64 s[12:13], s[0:1], 0
	v_add_f32_dpp v148, v152, v148 wave_shr:1 row_mask:0xf bank_mask:0xf bound_ctrl:1
	v_add_f32_dpp v149, v153, v149 wave_shr:1 row_mask:0xf bank_mask:0xf bound_ctrl:1
	v_pk_fma_f32 v[148:149], v[102:103], v[146:147], v[148:149] op_sel_hi:[1,0,1] neg_lo:[0,0,1] neg_hi:[0,0,1]
	v_pk_add_f32 v[148:149], v[148:149], v[90:91] neg_lo:[0,1] neg_hi:[0,1]
	v_pk_mul_f32 v[94:95], v[148:149], v[148:149]
	v_add_f32_e32 v94, v94, v95
	v_cndmask_b32_e64 v95, 0, v94, s[12:13]
	v_add_f32_e32 v1, v1, v95
	s_waitcnt vmcnt(4)
	v_mov_b32_dpp v8, v140 wave_shr:1 row_mask:0xf bank_mask:0xf bound_ctrl:1
	v_mov_b32_dpp v9, v141 wave_shr:1 row_mask:0xf bank_mask:0xf bound_ctrl:1
	v_mov_b32_dpp v10, v142 wave_shr:1 row_mask:0xf bank_mask:0xf bound_ctrl:1
	v_mov_b32_dpp v36, v140 wave_shl:1 row_mask:0xf bank_mask:0xf bound_ctrl:1
	v_mov_b32_dpp v37, v141 wave_shl:1 row_mask:0xf bank_mask:0xf bound_ctrl:1
	v_mov_b32_dpp v38, v142 wave_shl:1 row_mask:0xf bank_mask:0xf bound_ctrl:1
	s_add_i32 s4, s34, 11
	s_cmpk_lt_u32 s4, 0x201
	s_cselect_b64 s[12:13], s[40:41], 0
	v_cmp_eq_u32_e64 s[14:15], s37, v29
	s_and_b64 s[14:15], s[14:15], s[12:13]
	v_cndmask_b32_e64 v3, 0, 1, s[14:15]
	v_pk_add_f32 v[6:7], v[140:141], v[8:9]
	v_pk_mul_f32 v[62:63], v[140:141], v[140:141] op_sel_hi:[0,1]
	v_or_b32_dpp v16, v3, v3 wave_shr:1 row_mask:0xf bank_mask:0xf bound_ctrl:1
	v_pk_mul_f32 v[70:71], v[140:141], v[142:143] op_sel_hi:[1,0]
	v_or_b32_dpp v16, v3, v16 wave_shl:1 row_mask:0xf bank_mask:0xf bound_ctrl:1
	v_mul_f32_e64 v90, v141, v141
	v_mul_f32_e64 v91, v142, v142
	v_or_b32_dpp v76, v16, v16 wave_shr:1 row_mask:0xf bank_mask:0xf bound_ctrl:1
	v_add_f32_e64 v94, v142, v10
	v_pk_add_f32 v[6:7], v[6:7], v[36:37]
	v_or_b32_dpp v76, v16, v76 wave_shl:1 row_mask:0xf bank_mask:0xf bound_ctrl:1
	v_or3_b32 v3, v76, v87, v98
	v_or3_b32 v3, v3, v86, v77
	s_add_i32 s4, s34, 8
	s_cmpk_lt_u32 s4, 0x1ff
	s_cselect_b64 s[12:13], s[42:43], 0
	v_cmp_ne_u32_e64 s[30:31], 0, v3
	s_and_b64 s[30:31], s[30:31], s[12:13]
	v_cndmask_b32_e64 v3, 0, 1.0, s[30:31]
	v_pk_fma_f32 v[62:63], v[8:9], v[8:9], v[62:63] op_sel_hi:[0,1,1]
	v_pk_fma_f32 v[70:71], v[8:9], v[10:11], v[70:71] op_sel_hi:[1,0,1]
	v_fma_f32 v90, v9, v9, v90
	v_fma_f32 v91, v10, v10, v91
	v_add_f32_dpp v95, v3, v3 wave_shr:1 row_mask:0xf bank_mask:0xf bound_ctrl:1
	v_add_f32_e64 v94, v94, v38
	v_pk_fma_f32 v[62:63], v[36:37], v[36:37], v[62:63] op_sel_hi:[0,1,1]
	v_pk_fma_f32 v[70:71], v[36:37], v[38:39], v[70:71] op_sel_hi:[1,0,1]
	v_fma_f32 v90, v37, v37, v90
	v_fma_f32 v91, v38, v38, v91
	v_add_f32_dpp v95, v3, v95 wave_shl:1 row_mask:0xf bank_mask:0xf bound_ctrl:1
	v_pk_add_f32 v[112:113], v[4:5], v[6:7]
	v_pk_add_f32 v[102:103], v[46:47], v[112:113]
	v_pk_add_f32 v[46:47], v[24:25], v[62:63]
	v_pk_add_f32 v[4:5], v[68:69], v[46:47]
	v_pk_add_f32 v[24:25], v[44:45], v[70:71]
	v_pk_add_f32 v[68:69], v[78:79], v[24:25]
	v_pk_add_f32 v[78:79], v[52:53], v[90:91]
	v_pk_add_f32 v[44:45], v[92:93], v[78:79]
	v_pk_add_f32 v[110:111], v[58:59], v[94:95]
	v_pk_add_f32 v[52:53], v[96:97], v[110:111]
	v_mul_f32_e64 v124, v102, v22
	v_mul_f32_e64 v125, v103, v22
	v_mul_f32_e64 v126, v52, v22
	v_fma_f32 v3, v4, v22, v26
	v_mul_f32_e64 v16, v5, v22
	v_mul_f32_e64 v99, v68, v22
	v_fma_f32 v58, v44, v22, v26
	v_mul_f32_e64 v59, v69, v22
	v_fma_f32 v92, v45, v22, v26
	v_fma_f32 v3, -v124, v124, v3
	v_fma_f32 v16, -v124, v125, v16
	v_fma_f32 v99, -v124, v126, v99
	v_fma_f32 v58, -v125, v125, v58
	v_fma_f32 v59, -v125, v126, v59
	v_fma_f32 v92, -v126, v126, v92
	v_mul_f32_e64 v93, v59, v59
	v_mul_f32_e64 v96, v16, v92
	v_mul_f32_e64 v97, v99, v58
	v_mul_f32_e64 v114, v99, v99
	v_mul_f32_e64 v115, v3, v59
	v_mul_f32_e64 v118, v16, v16
	v_fma_f32 v93, v58, v92, -v93
	v_fma_f32 v96, v99, v59, -v96
	v_fma_f32 v97, v16, v59, -v97
	v_fma_f32 v114, v3, v92, -v114
	v_fma_f32 v115, v16, v99, -v115
	v_fma_f32 v118, v3, v58, -v118
	v_mul_f32_e64 v119, v3, v93
	v_fma_f32 v119, v16, v96, v119
	v_fma_f32 v119, v99, v97, v119
	v_rcp_f32_e32 v119, v119
	v_cmp_ne_u32_e64 vcc, s37, v17
	v_mul_f32_e64 v119, v119, v22
	v_cndmask_b32_e64 v119, 0, v119, s[30:31]
	v_cndmask_b32_e64 v3, 0, v18, vcc
	v_cndmask_b32_e64 v137, 0, v22, s[30:31]
	v_mul_f32_e64 v127, v93, v119
	v_mul_f32_e64 v132, v96, v119
	v_mul_f32_e64 v133, v97, v119
	v_mul_f32_e64 v134, v114, v119
	v_mul_f32_e64 v135, v115, v119
	v_mul_f32_e64 v136, v118, v119
	v_add_f32_e64 v138, v53, v3
	v_mov_b32_e32 v139, v17
	ds_write_b128 v23, v[124:127]
	ds_write_b128 v23, v[132:135] offset:1024
	ds_write_b128 v23, v[136:139] offset:2048
	v_mov_b32_dpp v58, v56 wave_shr:1 row_mask:0xf bank_mask:0xf bound_ctrl:1
	v_mov_b32_dpp v59, v57 wave_shr:1 row_mask:0xf bank_mask:0xf bound_ctrl:1
	v_mov_b32_dpp v102, v56 wave_shl:1 row_mask:0xf bank_mask:0xf bound_ctrl:1
	v_mov_b32_dpp v103, v57 wave_shl:1 row_mask:0xf bank_mask:0xf bound_ctrl:1
	v_pk_mul_f32 v[4:5], v[56:57], v[140:141] op_sel_hi:[1,0]
	v_pk_mul_f32 v[16:17], v[56:57], v[140:141] op_sel:[0,1]
	v_pk_mul_f32 v[44:45], v[56:57], v[142:143] op_sel_hi:[1,0]
	v_pk_add_f32 v[52:53], v[56:57], v[58:59]
	v_pk_fma_f32 v[4:5], v[58:59], v[8:9], v[4:5] op_sel_hi:[1,0,1]
	v_pk_fma_f32 v[16:17], v[58:59], v[8:9], v[16:17] op_sel:[0,1,0]
	v_pk_fma_f32 v[44:45], v[58:59], v[10:11], v[44:45] op_sel_hi:[1,0,1]
	v_pk_add_f32 v[52:53], v[52:53], v[102:103]
	v_pk_fma_f32 v[4:5], v[102:103], v[36:37], v[4:5] op_sel_hi:[1,0,1]
	v_pk_fma_f32 v[16:17], v[102:103], v[36:37], v[16:17] op_sel:[0,1,0]
	v_pk_fma_f32 v[44:45], v[102:103], v[38:39], v[44:45] op_sel_hi:[1,0,1]
	s_waitcnt lgkmcnt(0)
	s_barrier
	v_pk_add_f32 v[58:59], v[128:129], v[52:53]
	v_pk_add_f32 v[68:69], v[108:109], v[58:59]
	v_pk_add_f32 v[102:103], v[88:89], v[4:5]
	v_pk_add_f32 v[114:115], v[60:61], v[102:103]
	v_pk_add_f32 v[118:119], v[116:117], v[16:17]
	v_pk_add_f32 v[122:123], v[84:85], v[118:119]
	v_pk_add_f32 v[146:147], v[120:121], v[44:45]
	v_pk_add_f32 v[154:155], v[100:101], v[146:147]
	v_pk_fma_f32 v[114:115], v[124:125], v[68:69], v[114:115] op_sel_hi:[0,1,1] neg_lo:[1,0,0] neg_hi:[1,0,0]
	v_pk_fma_f32 v[122:123], v[124:125], v[68:69], v[122:123] op_sel:[1,0,0] neg_lo:[1,0,0] neg_hi:[1,0,0]
	v_pk_fma_f32 v[154:155], v[126:127], v[68:69], v[154:155] op_sel_hi:[0,1,1] neg_lo:[1,0,0] neg_hi:[1,0,0]
	v_pk_mul_f32 v[60:61], v[126:127], v[114:115] op_sel:[1,0]
	v_pk_mul_f32 v[84:85], v[132:133], v[114:115] op_sel_hi:[0,1]
	v_pk_mul_f32 v[88:89], v[132:133], v[114:115] op_sel:[1,0]
	v_pk_fma_f32 v[60:61], v[132:133], v[122:123], v[60:61] op_sel_hi:[0,1,1]
	v_pk_fma_f32 v[84:85], v[134:135], v[122:123], v[84:85] op_sel_hi:[0,1,1]
	v_pk_fma_f32 v[88:89], v[134:135], v[122:123], v[88:89] op_sel:[1,0,0]
	v_pk_fma_f32 v[60:61], v[132:133], v[154:155], v[60:61] op_sel:[1,0,0]
	v_pk_fma_f32 v[84:85], v[134:135], v[154:155], v[84:85] op_sel:[1,0,0]
	v_pk_fma_f32 v[88:89], v[136:137], v[154:155], v[88:89] op_sel_hi:[0,1,1]
	v_pk_mul_f32 v[162:163], v[124:125], v[60:61] op_sel_hi:[0,1]
	v_pk_fma_f32 v[162:163], v[124:125], v[84:85], v[162:163] op_sel:[1,0,0]
	v_pk_fma_f32 v[162:163], v[126:127], v[88:89], v[162:163] op_sel_hi:[0,1,1]
	v_pk_fma_f32 v[162:163], v[136:137], v[68:69], v[162:163] op_sel:[1,0,0] neg_lo:[0,0,1] neg_hi:[0,0,1]
	v_cmp_eq_u32_e64 s[10:11], 6, v139
	v_cmp_eq_u32_e64 s[14:15], 7, v139
	v_pk_add_f32 v[68:69], v[30:31], v[60:61]
	v_pk_add_f32 v[92:93], v[66:67], v[68:69]
	v_pk_add_f32 v[96:97], v[50:51], v[84:85]
	v_pk_add_f32 v[30:31], v[130:131], v[96:97]
	v_pk_add_f32 v[100:101], v[54:55], v[88:89]
	v_pk_add_f32 v[50:51], v[150:151], v[100:101]
	v_pk_add_f32 v[54:55], v[164:165], v[162:163]
	v_pk_add_f32 v[108:109], v[48:49], v[54:55]
	v_pk_fma_f32 v[48:49], v[12:13], v[92:93], v[108:109] op_sel_hi:[0,1,1]
	v_pk_fma_f32 v[116:117], v[80:81], v[92:93], v[108:109] op_sel_hi:[0,1,1]
	v_pk_fma_f32 v[48:49], v[12:13], v[30:31], v[48:49] op_sel:[1,0,0]
	v_pk_fma_f32 v[116:117], v[80:81], v[30:31], v[116:117] op_sel:[1,0,0]
	v_pk_fma_f32 v[48:49], v[14:15], v[50:51], v[48:49] op_sel_hi:[0,1,1]
	v_pk_fma_f32 v[116:117], v[82:83], v[50:51], v[116:117] op_sel_hi:[0,1,1]
	v_pk_fma_f32 v[108:109], v[168:169], v[92:93], v[108:109] op_sel_hi:[0,1,1]
	v_pk_fma_f32 v[108:109], v[168:169], v[30:31], v[108:109] op_sel:[1,0,0]
	v_pk_fma_f32 v[108:109], v[170:171], v[50:51], v[108:109] op_sel_hi:[0,1,1]
	v_cndmask_b32_e64 v66, 0, v18, s[10:11]
	v_cndmask_b32_e64 v67, 0, v18, s[14:15]
	v_add_f32_dpp v108, v48, v108 wave_shl:1 row_mask:0xf bank_mask:0xf bound_ctrl:1
	v_add_f32_dpp v109, v49, v109 wave_shl:1 row_mask:0xf bank_mask:0xf bound_ctrl:1
	s_add_i32 s4, s34, 8
	s_cmpk_lt_i32 s4, 0x201
	s_cselect_b64 s[12:13], s[0:1], 0
	v_add_f32_dpp v108, v116, v108 wave_shr:1 row_mask:0xf bank_mask:0xf bound_ctrl:1
	v_add_f32_dpp v109, v117, v109 wave_shr:1 row_mask:0xf bank_mask:0xf bound_ctrl:1
	v_pk_fma_f32 v[108:109], v[64:65], v[138:139], v[108:109] op_sel_hi:[1,0,1] neg_lo:[0,0,1] neg_hi:[0,0,1]
	v_pk_add_f32 v[108:109], v[108:109], v[66:67] neg_lo:[0,1] neg_hi:[0,1]
	v_pk_mul_f32 v[114:115], v[108:109], v[108:109]
	v_add_f32_e32 v114, v114, v115
	v_cndmask_b32_e64 v115, 0, v114, s[12:13]
	v_add_f32_e32 v1, v1, v115
	s_waitcnt vmcnt(0)
	v_mov_b32_dpp v12, v104 wave_shr:1 row_mask:0xf bank_mask:0xf bound_ctrl:1
	v_mov_b32_dpp v13, v105 wave_shr:1 row_mask:0xf bank_mask:0xf bound_ctrl:1
	v_mov_b32_dpp v14, v106 wave_shr:1 row_mask:0xf bank_mask:0xf bound_ctrl:1
	v_mov_b32_dpp v48, v104 wave_shl:1 row_mask:0xf bank_mask:0xf bound_ctrl:1
	v_mov_b32_dpp v49, v105 wave_shl:1 row_mask:0xf bank_mask:0xf bound_ctrl:1
	v_mov_b32_dpp v50, v106 wave_shl:1 row_mask:0xf bank_mask:0xf bound_ctrl:1
	s_add_i32 s4, s34, 12
	s_cmpk_lt_u32 s4, 0x201
	s_cselect_b64 s[12:13], s[40:41], 0
	v_cmp_eq_u32_e64 s[14:15], s37, v2
	s_and_b64 s[14:15], s[14:15], s[12:13]
	v_cndmask_b32_e64 v3, 0, 1, s[14:15]
	v_pk_add_f32 v[30:31], v[104:105], v[12:13]
	v_pk_mul_f32 v[64:65], v[104:105], v[104:105] op_sel_hi:[0,1]
	v_or_b32_dpp v77, v3, v3 wave_shr:1 row_mask:0xf bank_mask:0xf bound_ctrl:1
	v_pk_mul_f32 v[66:67], v[104:105], v[106:107] op_sel_hi:[1,0]
	v_or_b32_dpp v77, v3, v77 wave_shl:1 row_mask:0xf bank_mask:0xf bound_ctrl:1
	v_mul_f32_e64 v80, v105, v105
	v_mul_f32_e64 v81, v106, v106
	v_or_b32_dpp v99, v77, v77 wave_shr:1 row_mask:0xf bank_mask:0xf bound_ctrl:1
	v_add_f32_e64 v82, v106, v14
	v_pk_add_f32 v[30:31], v[30:31], v[48:49]
	v_or_b32_dpp v99, v77, v99 wave_shl:1 row_mask:0xf bank_mask:0xf bound_ctrl:1
	v_or3_b32 v3, v99, v76, v87
	v_or3_b32 v3, v3, v98, v86
	s_add_i32 s4, s34, 9
	s_cmpk_lt_u32 s4, 0x1ff
	s_cselect_b64 s[12:13], s[42:43], 0
	v_cmp_ne_u32_e64 s[30:31], 0, v3
	s_and_b64 s[30:31], s[30:31], s[12:13]
	v_cndmask_b32_e64 v3, 0, 1.0, s[30:31]
	v_pk_fma_f32 v[64:65], v[12:13], v[12:13], v[64:65] op_sel_hi:[0,1,1]
	v_pk_fma_f32 v[66:67], v[12:13], v[14:15], v[66:67] op_sel_hi:[1,0,1]
	v_fma_f32 v80, v13, v13, v80
	v_fma_f32 v81, v14, v14, v81
	v_add_f32_dpp v83, v3, v3 wave_shr:1 row_mask:0xf bank_mask:0xf bound_ctrl:1
	v_add_f32_e64 v82, v82, v50
	v_pk_fma_f32 v[64:65], v[48:49], v[48:49], v[64:65] op_sel_hi:[0,1,1]
	v_pk_fma_f32 v[66:67], v[48:49], v[50:51], v[66:67] op_sel_hi:[1,0,1]
	v_fma_f32 v80, v49, v49, v80
	v_fma_f32 v81, v50, v50, v81
	v_add_f32_dpp v83, v3, v83 wave_shl:1 row_mask:0xf bank_mask:0xf bound_ctrl:1
	v_pk_add_f32 v[92:93], v[112:113], v[30:31]
	v_pk_add_f32 v[108:109], v[46:47], v[64:65]
	v_pk_add_f32 v[46:47], v[24:25], v[66:67]
	v_pk_add_f32 v[24:25], v[78:79], v[80:81]
	v_pk_add_f32 v[78:79], v[110:111], v[82:83]
	v_mul_f32_e64 v112, v92, v22
	v_mul_f32_e64 v113, v93, v22
	v_mul_f32_e64 v114, v78, v22
	v_fma_f32 v3, v108, v22, v26
	v_mul_f32_e64 v77, v109, v22
	v_mul_f32_e64 v110, v46, v22
	v_fma_f32 v111, v24, v22, v26
	v_mul_f32_e64 v116, v47, v22
	v_fma_f32 v117, v25, v22, v26
	v_fma_f32 v3, -v112, v112, v3
	v_fma_f32 v77, -v112, v113, v77
	v_fma_f32 v110, -v112, v114, v110
	v_fma_f32 v111, -v113, v113, v111
	v_fma_f32 v116, -v113, v114, v116
	v_fma_f32 v117, -v114, v114, v117
	v_mul_f32_e64 v128, v116, v116
	v_mul_f32_e64 v129, v77, v117
	v_mul_f32_e64 v130, v110, v111
	v_mul_f32_e64 v131, v110, v110
	v_mul_f32_e64 v132, v3, v116
	v_mul_f32_e64 v133, v77, v77
	v_fma_f32 v128, v111, v117, -v128
	v_fma_f32 v129, v110, v116, -v129
	v_fma_f32 v130, v77, v116, -v130
	v_fma_f32 v131, v3, v117, -v131
	v_fma_f32 v132, v77, v110, -v132
	v_fma_f32 v133, v3, v111, -v133
	v_mul_f32_e64 v134, v3, v128
	v_fma_f32 v134, v77, v129, v134
	v_fma_f32 v134, v110, v130, v134
	v_rcp_f32_e32 v134, v134
	v_cmp_ne_u32_e64 vcc, s37, v43
	v_mul_f32_e64 v134, v134, v22
	v_cndmask_b32_e64 v134, 0, v134, s[30:31]
	v_cndmask_b32_e64 v3, 0, v18, vcc
	v_cndmask_b32_e64 v125, 0, v22, s[30:31]
	v_mul_f32_e64 v115, v128, v134
	v_mul_f32_e64 v120, v129, v134
	v_mul_f32_e64 v121, v130, v134
	v_mul_f32_e64 v122, v131, v134
	v_mul_f32_e64 v123, v132, v134
	v_mul_f32_e64 v124, v133, v134
	v_add_f32_e64 v126, v79, v3
	v_mov_b32_e32 v127, v43
	ds_write_b128 v23, v[112:115] offset:3072
	ds_write_b128 v23, v[120:123] offset:4096
	ds_write_b128 v23, v[124:127] offset:5120
	v_mov_b32_dpp v46, v40 wave_shr:1 row_mask:0xf bank_mask:0xf bound_ctrl:1
	v_mov_b32_dpp v47, v41 wave_shr:1 row_mask:0xf bank_mask:0xf bound_ctrl:1
	v_mov_b32_dpp v78, v40 wave_shl:1 row_mask:0xf bank_mask:0xf bound_ctrl:1
	v_mov_b32_dpp v79, v41 wave_shl:1 row_mask:0xf bank_mask:0xf bound_ctrl:1
	v_pk_mul_f32 v[24:25], v[40:41], v[104:105] op_sel_hi:[1,0]
	v_pk_mul_f32 v[92:93], v[40:41], v[104:105] op_sel:[0,1]
	v_pk_mul_f32 v[108:109], v[40:41], v[106:107] op_sel_hi:[1,0]
	v_pk_add_f32 v[116:117], v[40:41], v[46:47]
	v_pk_fma_f32 v[24:25], v[46:47], v[12:13], v[24:25] op_sel_hi:[1,0,1]
	v_pk_fma_f32 v[92:93], v[46:47], v[12:13], v[92:93] op_sel:[0,1,0]
	v_pk_fma_f32 v[108:109], v[46:47], v[14:15], v[108:109] op_sel_hi:[1,0,1]
	v_pk_add_f32 v[116:117], v[116:117], v[78:79]
	v_pk_fma_f32 v[24:25], v[78:79], v[48:49], v[24:25] op_sel_hi:[1,0,1]
	v_pk_fma_f32 v[92:93], v[78:79], v[48:49], v[92:93] op_sel:[0,1,0]
	v_pk_fma_f32 v[108:109], v[78:79], v[50:51], v[108:109] op_sel_hi:[1,0,1]
	s_waitcnt lgkmcnt(0)
	s_barrier
	v_pk_add_f32 v[46:47], v[58:59], v[116:117]
	v_pk_add_f32 v[128:129], v[102:103], v[24:25]
	v_pk_add_f32 v[132:133], v[118:119], v[92:93]
	v_pk_add_f32 v[136:137], v[146:147], v[108:109]
	v_pk_fma_f32 v[128:129], v[112:113], v[46:47], v[128:129] op_sel_hi:[0,1,1] neg_lo:[1,0,0] neg_hi:[1,0,0]
	v_pk_fma_f32 v[132:133], v[112:113], v[46:47], v[132:133] op_sel:[1,0,0] neg_lo:[1,0,0] neg_hi:[1,0,0]
	v_pk_fma_f32 v[136:137], v[114:115], v[46:47], v[136:137] op_sel_hi:[0,1,1] neg_lo:[1,0,0] neg_hi:[1,0,0]
	v_pk_mul_f32 v[58:59], v[114:115], v[128:129] op_sel:[1,0]
	v_pk_mul_f32 v[78:79], v[120:121], v[128:129] op_sel_hi:[0,1]
	v_pk_mul_f32 v[102:103], v[120:121], v[128:129] op_sel:[1,0]
	v_pk_fma_f32 v[58:59], v[120:121], v[132:133], v[58:59] op_sel_hi:[0,1,1]
	v_pk_fma_f32 v[78:79], v[122:123], v[132:133], v[78:79] op_sel_hi:[0,1,1]
	v_pk_fma_f32 v[102:103], v[122:123], v[132:133], v[102:103] op_sel:[1,0,0]
	v_pk_fma_f32 v[58:59], v[120:121], v[136:137], v[58:59] op_sel:[1,0,0]
	v_pk_fma_f32 v[78:79], v[122:123], v[136:137], v[78:79] op_sel:[1,0,0]
	v_pk_fma_f32 v[102:103], v[124:125], v[136:137], v[102:103] op_sel_hi:[0,1,1]
	v_pk_mul_f32 v[144:145], v[112:113], v[58:59] op_sel_hi:[0,1]
	v_pk_fma_f32 v[144:145], v[112:113], v[78:79], v[144:145] op_sel:[1,0,0]
	v_pk_fma_f32 v[144:145], v[114:115], v[102:103], v[144:145] op_sel_hi:[0,1,1]
	v_pk_fma_f32 v[144:145], v[124:125], v[46:47], v[144:145] op_sel:[1,0,0] neg_lo:[0,0,1] neg_hi:[0,0,1]
	v_cmp_eq_u32_e64 s[10:11], 6, v127
	v_cmp_eq_u32_e64 s[14:15], 7, v127
	v_pk_add_f32 v[46:47], v[68:69], v[58:59]
	v_pk_add_f32 v[68:69], v[96:97], v[78:79]
	v_pk_add_f32 v[96:97], v[100:101], v[102:103]
	v_pk_add_f32 v[110:111], v[54:55], v[144:145]
	v_pk_fma_f32 v[54:55], v[32:33], v[46:47], v[110:111] op_sel_hi:[0,1,1]
	v_pk_fma_f32 v[118:119], v[72:73], v[46:47], v[110:111] op_sel_hi:[0,1,1]
	v_pk_fma_f32 v[54:55], v[32:33], v[68:69], v[54:55] op_sel:[1,0,0]
	v_pk_fma_f32 v[118:119], v[72:73], v[68:69], v[118:119] op_sel:[1,0,0]
	v_pk_fma_f32 v[54:55], v[34:35], v[96:97], v[54:55] op_sel_hi:[0,1,1]
	v_pk_fma_f32 v[118:119], v[74:75], v[96:97], v[118:119] op_sel_hi:[0,1,1]
	v_pk_fma_f32 v[110:111], v[156:157], v[46:47], v[110:111] op_sel_hi:[0,1,1]
	v_pk_fma_f32 v[110:111], v[156:157], v[68:69], v[110:111] op_sel:[1,0,0]
	v_pk_fma_f32 v[110:111], v[158:159], v[96:97], v[110:111] op_sel_hi:[0,1,1]
	v_cndmask_b32_e64 v100, 0, v18, s[10:11]
	v_cndmask_b32_e64 v101, 0, v18, s[14:15]
	v_add_f32_dpp v110, v54, v110 wave_shl:1 row_mask:0xf bank_mask:0xf bound_ctrl:1
	v_add_f32_dpp v111, v55, v111 wave_shl:1 row_mask:0xf bank_mask:0xf bound_ctrl:1
	s_add_i32 s4, s34, 9
	s_cmpk_lt_i32 s4, 0x201
	s_cselect_b64 s[12:13], s[0:1], 0
	v_add_f32_dpp v110, v118, v110 wave_shr:1 row_mask:0xf bank_mask:0xf bound_ctrl:1
	v_add_f32_dpp v111, v119, v111 wave_shr:1 row_mask:0xf bank_mask:0xf bound_ctrl:1
	v_pk_fma_f32 v[110:111], v[20:21], v[126:127], v[110:111] op_sel_hi:[1,0,1] neg_lo:[0,0,1] neg_hi:[0,0,1]
	v_pk_add_f32 v[110:111], v[110:111], v[100:101] neg_lo:[0,1] neg_hi:[0,1]
	v_pk_mul_f32 v[128:129], v[110:111], v[110:111]
	v_add_f32_e32 v128, v128, v129
	v_cndmask_b32_e64 v129, 0, v128, s[12:13]
	v_add_f32_e32 v1, v1, v129
	v_mov_b32_e32 v0, v1
	s_branch .LBB0_29
